# P7 X1 tile loads nt
# baseline (speedup 1.0000x reference)
.LBB0_932:
	global_load_dwordx4 v[130:133], v[166:167], off offset:-1008 nt
	global_load_dwordx4 v[146:149], v[166:167], off offset:-1024 nt
	global_load_dwordx4 v[138:141], v[166:167], off offset:-880 nt
	global_load_dwordx4 v[142:145], v[166:167], off offset:-896 nt
	global_load_dwordx4 v[126:129], v[166:167], off offset:-752 nt
	global_load_dwordx4 v[134:137], v[166:167], off offset:-768 nt
	global_load_dwordx4 v[114:117], v[166:167], off offset:-624 nt
	global_load_dwordx4 v[122:125], v[166:167], off offset:-640 nt
	global_load_dwordx4 v[106:109], v[166:167], off offset:-496 nt
	global_load_dwordx4 v[110:113], v[166:167], off offset:-512 nt
	global_load_dwordx4 v[98:101], v[166:167], off offset:-368 nt
	global_load_dwordx4 v[102:105], v[166:167], off offset:-384 nt
	global_load_dwordx4 v[90:93], v[166:167], off offset:-240 nt
	global_load_dwordx4 v[94:97], v[166:167], off offset:-256 nt
	global_load_dwordx4 v[82:85], v[166:167], off offset:-112 nt
	global_load_dwordx4 v[86:89], v[166:167], off offset:-128 nt
	global_load_dwordx4 v[74:77], v[166:167], off offset:16 nt
	global_load_dwordx4 v[78:81], v[166:167], off nt
	global_load_dwordx4 v[66:69], v[166:167], off offset:144 nt
	global_load_dwordx4 v[70:73], v[166:167], off offset:128 nt
	global_load_dwordx4 v[58:61], v[166:167], off offset:272 nt
	global_load_dwordx4 v[62:65], v[166:167], off offset:256 nt
	global_load_dwordx4 v[34:37], v[166:167], off offset:400 nt
	global_load_dwordx4 v[38:41], v[166:167], off offset:384 nt
	s_waitcnt lgkmcnt(11)
	global_load_dwordx4 v[26:29], v[166:167], off offset:528 nt
	global_load_dwordx4 v[30:33], v[166:167], off offset:512 nt
	s_waitcnt lgkmcnt(7)
	global_load_dwordx4 v[18:21], v[166:167], off offset:656 nt
	global_load_dwordx4 v[22:25], v[166:167], off offset:640 nt
	s_waitcnt lgkmcnt(3)
	global_load_dwordx4 v[10:13], v[166:167], off offset:784 nt
	global_load_dwordx4 v[14:17], v[166:167], off offset:768 nt
	s_waitcnt lgkmcnt(0)
	global_load_dwordx4 v[2:5], v[166:167], off offset:912 nt
	global_load_dwordx4 v[6:9], v[166:167], off offset:896 nt
	v_add_u32_e32 v118, 0x10200, v169
	v_add_u32_e32 v150, 0x18300, v169
	v_add_u32_e32 v154, 0x10210, v169
	v_add_u32_e32 v158, 0x18310, v169
	ds_read_b128 v[42:45], v169
	ds_read_b128 v[46:49], v169 offset:16
	ds_read_b128 v[50:53], v169 offset:33024
	ds_read_b128 v[54:57], v169 offset:33040
	ds_read_b128 v[118:121], v118
	ds_read_b128 v[150:153], v150
	ds_read_b128 v[154:157], v154
	ds_read_b128 v[158:161], v158
	s_waitcnt vmcnt(30) lgkmcnt(7)
	v_mfma_f32_16x16x32_bf16 v[42:45], v[146:149], v[42:45], 0
	s_waitcnt lgkmcnt(5)
	v_mfma_f32_16x16x32_bf16 v[50:53], v[146:149], v[50:53], 0
	s_waitcnt lgkmcnt(3)
	v_mfma_f32_16x16x32_bf16 v[118:121], v[146:149], v[118:121], 0
	s_waitcnt lgkmcnt(2)
	v_mfma_f32_16x16x32_bf16 v[150:153], v[146:149], v[150:153], 0
	s_waitcnt lgkmcnt(1)
	v_mfma_f32_16x16x32_bf16 v[118:121], v[130:133], v[154:157], v[118:121]
	v_add_u32_e32 v154, 0x10280, v169
	v_add_u32_e32 v163, 0x18380, v169
	v_mfma_f32_16x16x32_bf16 v[42:45], v[130:133], v[46:49], v[42:45]
	v_mfma_f32_16x16x32_bf16 v[46:49], v[130:133], v[54:57], v[50:53]
	s_nop 2
	ds_read_b128 v[50:53], v169 offset:128
	ds_read_b128 v[54:57], v169 offset:33152
	ds_read_b128 v[154:157], v154
	ds_read_b128 v[242:245], v163
	s_waitcnt lgkmcnt(4)
	v_mfma_f32_16x16x32_bf16 v[150:153], v[130:133], v[158:161], v[150:153]
	s_waitcnt vmcnt(28) lgkmcnt(1)
	v_mfma_f32_16x16x32_bf16 v[118:121], v[142:145], v[154:157], v[118:121]
	v_add_u32_e32 v154, 0x10290, v169
	v_add_u32_e32 v158, 0x18390, v169
	v_mfma_f32_16x16x32_bf16 v[42:45], v[142:145], v[50:53], v[42:45]
	v_mfma_f32_16x16x32_bf16 v[46:49], v[142:145], v[54:57], v[46:49]
	ds_read_b128 v[50:53], v169 offset:144
	ds_read_b128 v[54:57], v169 offset:33168
	ds_read_b128 v[154:157], v154
	ds_read_b128 v[158:161], v158
	s_waitcnt lgkmcnt(4)
	v_mfma_f32_16x16x32_bf16 v[150:153], v[142:145], v[242:245], v[150:153]
	s_waitcnt lgkmcnt(3)
	v_mfma_f32_16x16x32_bf16 v[42:45], v[138:141], v[50:53], v[42:45]
	v_add_u32_e32 v163, 0x18400, v169
	s_waitcnt lgkmcnt(2)
	v_mfma_f32_16x16x32_bf16 v[46:49], v[138:141], v[54:57], v[46:49]
	s_waitcnt lgkmcnt(1)
	v_mfma_f32_16x16x32_bf16 v[50:53], v[138:141], v[154:157], v[118:121]
	ds_read_b128 v[54:57], v169 offset:256
	s_nop 1
	ds_read_b128 v[118:121], v169 offset:33280
	v_add_u32_e32 v154, 0x10300, v169
	ds_read_b128 v[154:157], v154
	ds_read_b128 v[242:245], v163
	s_waitcnt lgkmcnt(4)
	v_mfma_f32_16x16x32_bf16 v[150:153], v[138:141], v[158:161], v[150:153]
	s_waitcnt vmcnt(26) lgkmcnt(3)
	v_mfma_f32_16x16x32_bf16 v[42:45], v[134:137], v[54:57], v[42:45]
	s_waitcnt lgkmcnt(2)
	v_mfma_f32_16x16x32_bf16 v[46:49], v[134:137], v[118:121], v[46:49]
	s_waitcnt lgkmcnt(1)
	v_mfma_f32_16x16x32_bf16 v[50:53], v[134:137], v[154:157], v[50:53]
	ds_read_b128 v[54:57], v169 offset:272
	ds_read_b128 v[118:121], v169 offset:33296
	ds_read_b128 v[154:157], v254
	ds_read_b128 v[158:161], v173
	s_waitcnt lgkmcnt(4)
	v_mfma_f32_16x16x32_bf16 v[150:153], v[134:137], v[242:245], v[150:153]
	s_waitcnt lgkmcnt(3)
	v_mfma_f32_16x16x32_bf16 v[42:45], v[126:129], v[54:57], v[42:45]
	v_add_u32_e32 v163, 0x18480, v169
	s_waitcnt lgkmcnt(2)
	v_mfma_f32_16x16x32_bf16 v[46:49], v[126:129], v[118:121], v[46:49]
	ds_read_b128 v[54:57], v169 offset:384
	ds_read_b128 v[118:121], v169 offset:33408
	ds_read_b128 v[242:245], v163
	s_waitcnt lgkmcnt(4)
	v_mfma_f32_16x16x32_bf16 v[50:53], v[126:129], v[154:157], v[50:53]
	v_add_u32_e32 v154, 0x10380, v169
	ds_read_b128 v[154:157], v154
	s_waitcnt lgkmcnt(4)
	v_mfma_f32_16x16x32_bf16 v[150:153], v[126:129], v[158:161], v[150:153]
	s_waitcnt vmcnt(24) lgkmcnt(3)
	v_mfma_f32_16x16x32_bf16 v[42:45], v[122:125], v[54:57], v[42:45]
	s_waitcnt lgkmcnt(2)
	v_mfma_f32_16x16x32_bf16 v[46:49], v[122:125], v[118:121], v[46:49]
	s_waitcnt lgkmcnt(0)
	v_mfma_f32_16x16x32_bf16 v[50:53], v[122:125], v[154:157], v[50:53]
	ds_read_b128 v[54:57], v169 offset:400
	ds_read_b128 v[118:121], v169 offset:33424
	ds_read_b128 v[154:157], v178
	ds_read_b128 v[158:161], v179
	v_mfma_f32_16x16x32_bf16 v[150:153], v[122:125], v[242:245], v[150:153]
	s_waitcnt lgkmcnt(3)
	v_mfma_f32_16x16x32_bf16 v[42:45], v[114:117], v[54:57], v[42:45]
	s_waitcnt lgkmcnt(2)
	v_mfma_f32_16x16x32_bf16 v[46:49], v[114:117], v[118:121], v[46:49]
	s_waitcnt lgkmcnt(1)
	v_mfma_f32_16x16x32_bf16 v[50:53], v[114:117], v[154:157], v[50:53]
	ds_read_b128 v[54:57], v169 offset:512
	ds_read_b128 v[118:121], v169 offset:33536
	ds_read_b128 v[154:157], v180
	ds_read_b128 v[242:245], v181
	s_waitcnt lgkmcnt(4)
	v_mfma_f32_16x16x32_bf16 v[150:153], v[114:117], v[158:161], v[150:153]
	s_waitcnt vmcnt(22) lgkmcnt(3)
	v_mfma_f32_16x16x32_bf16 v[42:45], v[110:113], v[54:57], v[42:45]
	s_waitcnt lgkmcnt(2)
	v_mfma_f32_16x16x32_bf16 v[46:49], v[110:113], v[118:121], v[46:49]
	s_waitcnt lgkmcnt(1)
	v_mfma_f32_16x16x32_bf16 v[50:53], v[110:113], v[154:157], v[50:53]
	ds_read_b128 v[54:57], v169 offset:528
	ds_read_b128 v[118:121], v169 offset:33552
	ds_read_b128 v[154:157], v182
	ds_read_b128 v[158:161], v183
	s_waitcnt lgkmcnt(4)
	v_mfma_f32_16x16x32_bf16 v[150:153], v[110:113], v[242:245], v[150:153]
	s_waitcnt lgkmcnt(3)
	v_mfma_f32_16x16x32_bf16 v[42:45], v[106:109], v[54:57], v[42:45]
	s_waitcnt lgkmcnt(2)
	v_mfma_f32_16x16x32_bf16 v[46:49], v[106:109], v[118:121], v[46:49]
	s_waitcnt lgkmcnt(1)
	v_mfma_f32_16x16x32_bf16 v[50:53], v[106:109], v[154:157], v[50:53]
	ds_read_b128 v[54:57], v169 offset:640
	ds_read_b128 v[118:121], v169 offset:33664
	ds_read_b128 v[154:157], v184
	ds_read_b128 v[242:245], v185
	s_waitcnt lgkmcnt(4)
	v_mfma_f32_16x16x32_bf16 v[150:153], v[106:109], v[158:161], v[150:153]
	s_waitcnt vmcnt(20) lgkmcnt(3)
	v_mfma_f32_16x16x32_bf16 v[42:45], v[102:105], v[54:57], v[42:45]
	s_waitcnt lgkmcnt(2)
	v_mfma_f32_16x16x32_bf16 v[46:49], v[102:105], v[118:121], v[46:49]
	s_waitcnt lgkmcnt(1)
	v_mfma_f32_16x16x32_bf16 v[50:53], v[102:105], v[154:157], v[50:53]
	ds_read_b128 v[54:57], v169 offset:656
	ds_read_b128 v[118:121], v169 offset:33680
	ds_read_b128 v[154:157], v186
	ds_read_b128 v[158:161], v187
	s_waitcnt lgkmcnt(4)
	v_mfma_f32_16x16x32_bf16 v[150:153], v[102:105], v[242:245], v[150:153]
	s_waitcnt lgkmcnt(3)
	v_mfma_f32_16x16x32_bf16 v[42:45], v[98:101], v[54:57], v[42:45]
	s_waitcnt lgkmcnt(2)
	v_mfma_f32_16x16x32_bf16 v[46:49], v[98:101], v[118:121], v[46:49]
	s_waitcnt lgkmcnt(1)
	v_mfma_f32_16x16x32_bf16 v[50:53], v[98:101], v[154:157], v[50:53]
	ds_read_b128 v[54:57], v169 offset:768
	ds_read_b128 v[118:121], v169 offset:33792
	ds_read_b128 v[154:157], v188
	ds_read_b128 v[242:245], v189
	s_waitcnt lgkmcnt(4)
	v_mfma_f32_16x16x32_bf16 v[150:153], v[98:101], v[158:161], v[150:153]
	s_waitcnt vmcnt(18) lgkmcnt(3)
	v_mfma_f32_16x16x32_bf16 v[42:45], v[94:97], v[54:57], v[42:45]
	s_waitcnt lgkmcnt(2)
	v_mfma_f32_16x16x32_bf16 v[46:49], v[94:97], v[118:121], v[46:49]
	s_waitcnt lgkmcnt(1)
	v_mfma_f32_16x16x32_bf16 v[50:53], v[94:97], v[154:157], v[50:53]
	ds_read_b128 v[54:57], v169 offset:784
	ds_read_b128 v[118:121], v169 offset:33808
	ds_read_b128 v[154:157], v190
	ds_read_b128 v[158:161], v191
	s_waitcnt lgkmcnt(4)
	v_mfma_f32_16x16x32_bf16 v[150:153], v[94:97], v[242:245], v[150:153]
	s_waitcnt lgkmcnt(3)
	v_mfma_f32_16x16x32_bf16 v[42:45], v[90:93], v[54:57], v[42:45]
	s_waitcnt lgkmcnt(2)
	v_mfma_f32_16x16x32_bf16 v[46:49], v[90:93], v[118:121], v[46:49]
	s_waitcnt lgkmcnt(1)
	v_mfma_f32_16x16x32_bf16 v[50:53], v[90:93], v[154:157], v[50:53]
	ds_read_b128 v[54:57], v169 offset:896
	ds_read_b128 v[118:121], v169 offset:33920
	ds_read_b128 v[154:157], v192
	ds_read_b128 v[242:245], v193
	s_waitcnt lgkmcnt(4)
	v_mfma_f32_16x16x32_bf16 v[150:153], v[90:93], v[158:161], v[150:153]
	s_waitcnt vmcnt(16) lgkmcnt(3)
	v_mfma_f32_16x16x32_bf16 v[42:45], v[86:89], v[54:57], v[42:45]
	s_waitcnt lgkmcnt(2)
	v_mfma_f32_16x16x32_bf16 v[46:49], v[86:89], v[118:121], v[46:49]
	s_waitcnt lgkmcnt(1)
	v_mfma_f32_16x16x32_bf16 v[50:53], v[86:89], v[154:157], v[50:53]
	ds_read_b128 v[54:57], v169 offset:912
	ds_read_b128 v[118:121], v169 offset:33936
	ds_read_b128 v[154:157], v194
	ds_read_b128 v[158:161], v195
	s_waitcnt lgkmcnt(4)
	v_mfma_f32_16x16x32_bf16 v[150:153], v[86:89], v[242:245], v[150:153]
	s_waitcnt lgkmcnt(3)
	v_mfma_f32_16x16x32_bf16 v[42:45], v[82:85], v[54:57], v[42:45]
	s_waitcnt lgkmcnt(2)
	v_mfma_f32_16x16x32_bf16 v[46:49], v[82:85], v[118:121], v[46:49]
	s_waitcnt lgkmcnt(1)
	v_mfma_f32_16x16x32_bf16 v[50:53], v[82:85], v[154:157], v[50:53]
	ds_read_b128 v[54:57], v169 offset:1024
	ds_read_b128 v[118:121], v169 offset:34048
	ds_read_b128 v[154:157], v196
	ds_read_b128 v[242:245], v197
	s_waitcnt lgkmcnt(4)
	v_mfma_f32_16x16x32_bf16 v[150:153], v[82:85], v[158:161], v[150:153]
	s_waitcnt vmcnt(14) lgkmcnt(3)
	v_mfma_f32_16x16x32_bf16 v[42:45], v[78:81], v[54:57], v[42:45]
	s_waitcnt lgkmcnt(2)
	v_mfma_f32_16x16x32_bf16 v[46:49], v[78:81], v[118:121], v[46:49]
	s_waitcnt lgkmcnt(1)
	v_mfma_f32_16x16x32_bf16 v[50:53], v[78:81], v[154:157], v[50:53]
	ds_read_b128 v[54:57], v169 offset:1040
	ds_read_b128 v[118:121], v169 offset:34064
	ds_read_b128 v[154:157], v198
	ds_read_b128 v[158:161], v199
	s_waitcnt lgkmcnt(4)
	v_mfma_f32_16x16x32_bf16 v[150:153], v[78:81], v[242:245], v[150:153]
	s_waitcnt lgkmcnt(3)
	v_mfma_f32_16x16x32_bf16 v[42:45], v[74:77], v[54:57], v[42:45]
	s_waitcnt lgkmcnt(2)
	v_mfma_f32_16x16x32_bf16 v[46:49], v[74:77], v[118:121], v[46:49]
	s_waitcnt lgkmcnt(1)
	v_mfma_f32_16x16x32_bf16 v[50:53], v[74:77], v[154:157], v[50:53]
	ds_read_b128 v[54:57], v169 offset:1152
	ds_read_b128 v[118:121], v169 offset:34176
	ds_read_b128 v[154:157], v200
	ds_read_b128 v[242:245], v201
	s_waitcnt lgkmcnt(4)
	v_mfma_f32_16x16x32_bf16 v[150:153], v[74:77], v[158:161], v[150:153]
	s_waitcnt vmcnt(12) lgkmcnt(3)
	v_mfma_f32_16x16x32_bf16 v[42:45], v[70:73], v[54:57], v[42:45]
	s_waitcnt lgkmcnt(2)
	v_mfma_f32_16x16x32_bf16 v[46:49], v[70:73], v[118:121], v[46:49]
	s_waitcnt lgkmcnt(1)
	v_mfma_f32_16x16x32_bf16 v[50:53], v[70:73], v[154:157], v[50:53]
	ds_read_b128 v[54:57], v169 offset:1168
	ds_read_b128 v[118:121], v169 offset:34192
	ds_read_b128 v[154:157], v202
	ds_read_b128 v[158:161], v203
	s_waitcnt lgkmcnt(4)
	v_mfma_f32_16x16x32_bf16 v[150:153], v[70:73], v[242:245], v[150:153]
	s_waitcnt lgkmcnt(3)
	v_mfma_f32_16x16x32_bf16 v[42:45], v[66:69], v[54:57], v[42:45]
	s_waitcnt lgkmcnt(2)
	v_mfma_f32_16x16x32_bf16 v[46:49], v[66:69], v[118:121], v[46:49]
	s_waitcnt lgkmcnt(1)
	v_mfma_f32_16x16x32_bf16 v[50:53], v[66:69], v[154:157], v[50:53]
	ds_read_b128 v[54:57], v169 offset:1280
	ds_read_b128 v[118:121], v169 offset:34304
	ds_read_b128 v[154:157], v204
	ds_read_b128 v[242:245], v205
	s_waitcnt lgkmcnt(4)
	v_mfma_f32_16x16x32_bf16 v[150:153], v[66:69], v[158:161], v[150:153]
	s_waitcnt vmcnt(10) lgkmcnt(3)
	v_mfma_f32_16x16x32_bf16 v[42:45], v[62:65], v[54:57], v[42:45]
	s_waitcnt lgkmcnt(2)
	v_mfma_f32_16x16x32_bf16 v[46:49], v[62:65], v[118:121], v[46:49]
	s_waitcnt lgkmcnt(1)
	v_mfma_f32_16x16x32_bf16 v[50:53], v[62:65], v[154:157], v[50:53]
	ds_read_b128 v[54:57], v169 offset:1296
	ds_read_b128 v[118:121], v169 offset:34320
	ds_read_b128 v[154:157], v206
	ds_read_b128 v[158:161], v207
	s_waitcnt lgkmcnt(4)
	v_mfma_f32_16x16x32_bf16 v[150:153], v[62:65], v[242:245], v[150:153]
	s_waitcnt lgkmcnt(3)
	v_mfma_f32_16x16x32_bf16 v[42:45], v[58:61], v[54:57], v[42:45]
	s_waitcnt lgkmcnt(2)
	v_mfma_f32_16x16x32_bf16 v[46:49], v[58:61], v[118:121], v[46:49]
	s_waitcnt lgkmcnt(1)
	v_mfma_f32_16x16x32_bf16 v[50:53], v[58:61], v[154:157], v[50:53]
	ds_read_b128 v[54:57], v169 offset:1408
	ds_read_b128 v[118:121], v169 offset:34432
	ds_read_b128 v[154:157], v208
	ds_read_b128 v[242:245], v209
	s_waitcnt lgkmcnt(4)
	v_mfma_f32_16x16x32_bf16 v[150:153], v[58:61], v[158:161], v[150:153]
	s_waitcnt vmcnt(8) lgkmcnt(3)
	v_mfma_f32_16x16x32_bf16 v[42:45], v[38:41], v[54:57], v[42:45]
	s_waitcnt lgkmcnt(2)
	v_mfma_f32_16x16x32_bf16 v[46:49], v[38:41], v[118:121], v[46:49]
	s_waitcnt lgkmcnt(1)
	v_mfma_f32_16x16x32_bf16 v[50:53], v[38:41], v[154:157], v[50:53]
	ds_read_b128 v[54:57], v169 offset:1424
	ds_read_b128 v[118:121], v169 offset:34448
	ds_read_b128 v[154:157], v210
	ds_read_b128 v[158:161], v211
	s_waitcnt lgkmcnt(4)
	v_mfma_f32_16x16x32_bf16 v[150:153], v[38:41], v[242:245], v[150:153]
	s_waitcnt lgkmcnt(3)
	v_mfma_f32_16x16x32_bf16 v[42:45], v[34:37], v[54:57], v[42:45]
	s_waitcnt lgkmcnt(2)
	v_mfma_f32_16x16x32_bf16 v[46:49], v[34:37], v[118:121], v[46:49]
	s_waitcnt lgkmcnt(1)
	v_mfma_f32_16x16x32_bf16 v[50:53], v[34:37], v[154:157], v[50:53]
	ds_read_b128 v[54:57], v169 offset:1536
	ds_read_b128 v[118:121], v169 offset:34560
	ds_read_b128 v[154:157], v212
	ds_read_b128 v[242:245], v213
	s_waitcnt lgkmcnt(4)
	v_mfma_f32_16x16x32_bf16 v[150:153], v[34:37], v[158:161], v[150:153]
	s_waitcnt vmcnt(6) lgkmcnt(3)
	v_mfma_f32_16x16x32_bf16 v[42:45], v[30:33], v[54:57], v[42:45]
	s_waitcnt lgkmcnt(2)
	v_mfma_f32_16x16x32_bf16 v[46:49], v[30:33], v[118:121], v[46:49]
	s_waitcnt lgkmcnt(1)
	v_mfma_f32_16x16x32_bf16 v[50:53], v[30:33], v[154:157], v[50:53]
	ds_read_b128 v[54:57], v169 offset:1552
	ds_read_b128 v[118:121], v169 offset:34576
	ds_read_b128 v[154:157], v214
	ds_read_b128 v[158:161], v215
	s_waitcnt lgkmcnt(4)
	v_mfma_f32_16x16x32_bf16 v[150:153], v[30:33], v[242:245], v[150:153]
	s_waitcnt lgkmcnt(3)
	v_mfma_f32_16x16x32_bf16 v[42:45], v[26:29], v[54:57], v[42:45]
	s_waitcnt lgkmcnt(2)
	v_mfma_f32_16x16x32_bf16 v[46:49], v[26:29], v[118:121], v[46:49]
	s_waitcnt lgkmcnt(1)
	v_mfma_f32_16x16x32_bf16 v[50:53], v[26:29], v[154:157], v[50:53]
	ds_read_b128 v[54:57], v169 offset:1664
	ds_read_b128 v[118:121], v169 offset:34688
	ds_read_b128 v[154:157], v216
	ds_read_b128 v[242:245], v217
	s_waitcnt lgkmcnt(4)
	v_mfma_f32_16x16x32_bf16 v[150:153], v[26:29], v[158:161], v[150:153]
	s_waitcnt vmcnt(4) lgkmcnt(3)
	v_mfma_f32_16x16x32_bf16 v[42:45], v[22:25], v[54:57], v[42:45]
	s_waitcnt lgkmcnt(2)
	v_mfma_f32_16x16x32_bf16 v[46:49], v[22:25], v[118:121], v[46:49]
	s_waitcnt lgkmcnt(1)
	v_mfma_f32_16x16x32_bf16 v[50:53], v[22:25], v[154:157], v[50:53]
	ds_read_b128 v[54:57], v169 offset:1680
	ds_read_b128 v[118:121], v169 offset:34704
	ds_read_b128 v[154:157], v218
	ds_read_b128 v[158:161], v219
	s_waitcnt lgkmcnt(4)
	v_mfma_f32_16x16x32_bf16 v[150:153], v[22:25], v[242:245], v[150:153]
	s_waitcnt lgkmcnt(3)
	v_mfma_f32_16x16x32_bf16 v[42:45], v[18:21], v[54:57], v[42:45]
	s_waitcnt lgkmcnt(2)
	v_mfma_f32_16x16x32_bf16 v[46:49], v[18:21], v[118:121], v[46:49]
	s_waitcnt lgkmcnt(1)
	v_mfma_f32_16x16x32_bf16 v[50:53], v[18:21], v[154:157], v[50:53]
	ds_read_b128 v[54:57], v169 offset:1792
	ds_read_b128 v[118:121], v169 offset:34816
	ds_read_b128 v[154:157], v220
	ds_read_b128 v[242:245], v221
	s_waitcnt lgkmcnt(4)
	v_mfma_f32_16x16x32_bf16 v[150:153], v[18:21], v[158:161], v[150:153]
	s_waitcnt vmcnt(2) lgkmcnt(3)
	v_mfma_f32_16x16x32_bf16 v[42:45], v[14:17], v[54:57], v[42:45]
	s_waitcnt lgkmcnt(2)
	v_mfma_f32_16x16x32_bf16 v[46:49], v[14:17], v[118:121], v[46:49]
	s_waitcnt lgkmcnt(1)
	v_mfma_f32_16x16x32_bf16 v[50:53], v[14:17], v[154:157], v[50:53]
	ds_read_b128 v[54:57], v169 offset:1808
	ds_read_b128 v[118:121], v169 offset:34832
	ds_read_b128 v[154:157], v222
	ds_read_b128 v[158:161], v223
	s_waitcnt lgkmcnt(4)
	v_mfma_f32_16x16x32_bf16 v[150:153], v[14:17], v[242:245], v[150:153]
	s_waitcnt lgkmcnt(3)
	v_mfma_f32_16x16x32_bf16 v[42:45], v[10:13], v[54:57], v[42:45]
	s_waitcnt lgkmcnt(1)
	v_mfma_f32_16x16x32_bf16 v[50:53], v[10:13], v[154:157], v[50:53]
	ds_read_b128 v[54:57], v169 offset:1920
	ds_read_b128 v[154:157], v169 offset:34944
	ds_read_b128 v[242:245], v224
	ds_read_b128 v[246:249], v225
	v_mfma_f32_16x16x32_bf16 v[46:49], v[10:13], v[118:121], v[46:49]
	s_waitcnt lgkmcnt(4)
	v_mfma_f32_16x16x32_bf16 v[250:253], v[10:13], v[158:161], v[150:153]
	s_waitcnt vmcnt(0) lgkmcnt(3)
	v_mfma_f32_16x16x32_bf16 v[118:121], v[6:9], v[54:57], v[42:45]
	s_waitcnt lgkmcnt(2)
	v_mfma_f32_16x16x32_bf16 v[42:45], v[6:9], v[154:157], v[46:49]
	s_waitcnt lgkmcnt(1)
	v_mfma_f32_16x16x32_bf16 v[150:153], v[6:9], v[242:245], v[50:53]
	ds_read_b128 v[158:161], v169 offset:1936
	ds_read_b128 v[46:49], v169 offset:34960
	ds_read_b128 v[154:157], v226
	ds_read_b128 v[50:53], v227
	s_waitcnt lgkmcnt(4)
	v_mfma_f32_16x16x32_bf16 v[54:57], v[6:9], v[246:249], v[250:253]
	v_lshlrev_b32_e32 v175, 16, v147
	v_lshlrev_b32_e32 v174, 16, v146
	v_pk_fma_f32 v[174:175], v[174:175], v[174:175], 0 op_sel_hi:[1,1,0]
	v_lshlrev_b32_e32 v177, 16, v149
	v_lshlrev_b32_e32 v176, 16, v148
	v_pk_fma_f32 v[174:175], v[176:177], v[176:177], v[174:175]
	v_lshlrev_b32_e32 v177, 16, v131
	v_lshlrev_b32_e32 v176, 16, v130
	v_pk_fma_f32 v[174:175], v[176:177], v[176:177], v[174:175]
	v_lshlrev_b32_e32 v177, 16, v133
	v_lshlrev_b32_e32 v176, 16, v132
	v_pk_fma_f32 v[174:175], v[176:177], v[176:177], v[174:175]
	v_lshlrev_b32_e32 v177, 16, v143
	v_lshlrev_b32_e32 v176, 16, v142
	v_pk_fma_f32 v[174:175], v[176:177], v[176:177], v[174:175]
	v_lshlrev_b32_e32 v177, 16, v145
	v_lshlrev_b32_e32 v176, 16, v144
	v_pk_fma_f32 v[174:175], v[176:177], v[176:177], v[174:175]
	v_lshlrev_b32_e32 v177, 16, v139
	v_lshlrev_b32_e32 v176, 16, v138
	v_pk_fma_f32 v[174:175], v[176:177], v[176:177], v[174:175]
	v_lshlrev_b32_e32 v177, 16, v141
	v_lshlrev_b32_e32 v176, 16, v140
	v_pk_fma_f32 v[174:175], v[176:177], v[176:177], v[174:175]
	v_lshlrev_b32_e32 v177, 16, v135
	v_lshlrev_b32_e32 v176, 16, v134
	v_pk_fma_f32 v[174:175], v[176:177], v[176:177], v[174:175]
	v_and_b32_e32 v177, 0xffff0000, v147
	v_and_b32_e32 v176, 0xffff0000, v146
	v_pk_fma_f32 v[176:177], v[176:177], v[176:177], 0 op_sel_hi:[1,1,0]
	v_and_b32_e32 v243, 0xffff0000, v149
	v_and_b32_e32 v242, 0xffff0000, v148
	v_pk_fma_f32 v[176:177], v[242:243], v[242:243], v[176:177]
	v_and_b32_e32 v243, 0xffff0000, v131
	v_and_b32_e32 v242, 0xffff0000, v130
	v_pk_fma_f32 v[176:177], v[242:243], v[242:243], v[176:177]
	v_and_b32_e32 v243, 0xffff0000, v133
	v_and_b32_e32 v242, 0xffff0000, v132
	v_pk_fma_f32 v[176:177], v[242:243], v[242:243], v[176:177]
	v_and_b32_e32 v243, 0xffff0000, v143
	v_and_b32_e32 v242, 0xffff0000, v142
	v_pk_fma_f32 v[176:177], v[242:243], v[242:243], v[176:177]
	v_and_b32_e32 v243, 0xffff0000, v145
	v_and_b32_e32 v242, 0xffff0000, v144
	v_pk_fma_f32 v[176:177], v[242:243], v[242:243], v[176:177]
	v_and_b32_e32 v243, 0xffff0000, v139
	v_and_b32_e32 v242, 0xffff0000, v138
	v_pk_fma_f32 v[176:177], v[242:243], v[242:243], v[176:177]
	v_and_b32_e32 v243, 0xffff0000, v141
	v_and_b32_e32 v242, 0xffff0000, v140
	v_pk_fma_f32 v[176:177], v[242:243], v[242:243], v[176:177]
	v_and_b32_e32 v243, 0xffff0000, v135
	v_and_b32_e32 v242, 0xffff0000, v134
	v_pk_fma_f32 v[176:177], v[242:243], v[242:243], v[176:177]
	v_lshlrev_b32_e32 v243, 16, v137
	v_lshlrev_b32_e32 v242, 16, v136
	v_lshlrev_b32_e32 v246, 16, v126
	v_lshlrev_b32_e32 v247, 16, v127
	v_pk_fma_f32 v[174:175], v[242:243], v[242:243], v[174:175]
	v_lshlrev_b32_e32 v243, 16, v129
	v_pk_fma_f32 v[174:175], v[246:247], v[246:247], v[174:175]
	v_lshlrev_b32_e32 v242, 16, v128
	v_pk_fma_f32 v[174:175], v[242:243], v[242:243], v[174:175]
	v_lshlrev_b32_e32 v243, 16, v123
	v_lshlrev_b32_e32 v242, 16, v122
	v_pk_fma_f32 v[174:175], v[242:243], v[242:243], v[174:175]
	v_lshlrev_b32_e32 v243, 16, v125
	v_lshlrev_b32_e32 v242, 16, v124
	v_pk_fma_f32 v[174:175], v[242:243], v[242:243], v[174:175]
	v_lshlrev_b32_e32 v243, 16, v115
	v_lshlrev_b32_e32 v242, 16, v114
	v_pk_fma_f32 v[174:175], v[242:243], v[242:243], v[174:175]
	v_lshlrev_b32_e32 v243, 16, v117
	v_lshlrev_b32_e32 v242, 16, v116
	v_pk_fma_f32 v[174:175], v[242:243], v[242:243], v[174:175]
	v_lshlrev_b32_e32 v243, 16, v111
	v_lshlrev_b32_e32 v242, 16, v110
	v_pk_fma_f32 v[174:175], v[242:243], v[242:243], v[174:175]
	v_lshlrev_b32_e32 v243, 16, v113
	v_lshlrev_b32_e32 v242, 16, v112
	v_and_b32_e32 v245, 0xffff0000, v137
	v_and_b32_e32 v244, 0xffff0000, v136
	v_pk_fma_f32 v[174:175], v[242:243], v[242:243], v[174:175]
	v_lshlrev_b32_e32 v243, 16, v107
	v_lshlrev_b32_e32 v242, 16, v106
	v_and_b32_e32 v248, 0xffff0000, v126
	v_and_b32_e32 v249, 0xffff0000, v127
	v_pk_fma_f32 v[174:175], v[242:243], v[242:243], v[174:175]
	v_lshlrev_b32_e32 v243, 16, v109
	v_lshlrev_b32_e32 v242, 16, v108
	v_pk_fma_f32 v[176:177], v[244:245], v[244:245], v[176:177]
	v_pk_fma_f32 v[174:175], v[242:243], v[242:243], v[174:175]
	v_pk_fma_f32 v[176:177], v[248:249], v[248:249], v[176:177]
	v_and_b32_e32 v243, 0xffff0000, v129
	v_and_b32_e32 v242, 0xffff0000, v128
	v_pk_fma_f32 v[176:177], v[242:243], v[242:243], v[176:177]
	v_and_b32_e32 v243, 0xffff0000, v123
	v_and_b32_e32 v242, 0xffff0000, v122
	v_pk_fma_f32 v[176:177], v[242:243], v[242:243], v[176:177]
	v_and_b32_e32 v243, 0xffff0000, v125
	v_and_b32_e32 v242, 0xffff0000, v124
	v_pk_fma_f32 v[176:177], v[242:243], v[242:243], v[176:177]
	v_and_b32_e32 v243, 0xffff0000, v115
	v_and_b32_e32 v242, 0xffff0000, v114
	v_pk_fma_f32 v[176:177], v[242:243], v[242:243], v[176:177]
	v_and_b32_e32 v243, 0xffff0000, v117
	v_and_b32_e32 v242, 0xffff0000, v116
	v_pk_fma_f32 v[176:177], v[242:243], v[242:243], v[176:177]
	v_and_b32_e32 v243, 0xffff0000, v111
	v_and_b32_e32 v242, 0xffff0000, v110
	v_pk_fma_f32 v[176:177], v[242:243], v[242:243], v[176:177]
	v_and_b32_e32 v243, 0xffff0000, v113
	v_and_b32_e32 v242, 0xffff0000, v112
	v_pk_fma_f32 v[176:177], v[242:243], v[242:243], v[176:177]
	v_and_b32_e32 v243, 0xffff0000, v107
	v_and_b32_e32 v242, 0xffff0000, v106
	v_pk_fma_f32 v[176:177], v[242:243], v[242:243], v[176:177]
	v_and_b32_e32 v243, 0xffff0000, v109
	v_and_b32_e32 v242, 0xffff0000, v108
	v_pk_fma_f32 v[176:177], v[242:243], v[242:243], v[176:177]
	v_lshlrev_b32_e32 v243, 16, v103
	v_lshlrev_b32_e32 v242, 16, v102
	v_lshlrev_b32_e32 v246, 16, v104
	v_lshlrev_b32_e32 v247, 16, v105
	v_pk_fma_f32 v[174:175], v[242:243], v[242:243], v[174:175]
	v_lshlrev_b32_e32 v243, 16, v99
	v_pk_fma_f32 v[174:175], v[246:247], v[246:247], v[174:175]
	v_lshlrev_b32_e32 v242, 16, v98
	v_pk_fma_f32 v[174:175], v[242:243], v[242:243], v[174:175]
	v_lshlrev_b32_e32 v243, 16, v101
	v_lshlrev_b32_e32 v242, 16, v100
	v_pk_fma_f32 v[174:175], v[242:243], v[242:243], v[174:175]
	v_lshlrev_b32_e32 v243, 16, v95
	v_lshlrev_b32_e32 v242, 16, v94
	v_pk_fma_f32 v[174:175], v[242:243], v[242:243], v[174:175]
	v_lshlrev_b32_e32 v243, 16, v97
	v_lshlrev_b32_e32 v242, 16, v96
	v_pk_fma_f32 v[174:175], v[242:243], v[242:243], v[174:175]
	v_lshlrev_b32_e32 v243, 16, v91
	v_lshlrev_b32_e32 v242, 16, v90
	v_pk_fma_f32 v[174:175], v[242:243], v[242:243], v[174:175]
	v_lshlrev_b32_e32 v243, 16, v93
	v_lshlrev_b32_e32 v242, 16, v92
	v_pk_fma_f32 v[174:175], v[242:243], v[242:243], v[174:175]
	v_lshlrev_b32_e32 v243, 16, v87
	v_lshlrev_b32_e32 v242, 16, v86
	v_and_b32_e32 v245, 0xffff0000, v103
	v_and_b32_e32 v244, 0xffff0000, v102
	v_pk_fma_f32 v[174:175], v[242:243], v[242:243], v[174:175]
	v_lshlrev_b32_e32 v243, 16, v89
	v_lshlrev_b32_e32 v242, 16, v88
	v_and_b32_e32 v248, 0xffff0000, v104
	v_and_b32_e32 v249, 0xffff0000, v105
	v_pk_fma_f32 v[174:175], v[242:243], v[242:243], v[174:175]
	v_lshlrev_b32_e32 v243, 16, v83
	v_lshlrev_b32_e32 v242, 16, v82
	v_pk_fma_f32 v[176:177], v[244:245], v[244:245], v[176:177]
	v_pk_fma_f32 v[174:175], v[242:243], v[242:243], v[174:175]
	v_pk_fma_f32 v[176:177], v[248:249], v[248:249], v[176:177]
	v_and_b32_e32 v243, 0xffff0000, v99
	v_and_b32_e32 v242, 0xffff0000, v98
	v_pk_fma_f32 v[176:177], v[242:243], v[242:243], v[176:177]
	v_and_b32_e32 v243, 0xffff0000, v101
	v_and_b32_e32 v242, 0xffff0000, v100
	v_pk_fma_f32 v[176:177], v[242:243], v[242:243], v[176:177]
	v_and_b32_e32 v243, 0xffff0000, v95
	v_and_b32_e32 v242, 0xffff0000, v94
	v_pk_fma_f32 v[176:177], v[242:243], v[242:243], v[176:177]
	v_and_b32_e32 v243, 0xffff0000, v97
	v_and_b32_e32 v242, 0xffff0000, v96
	v_pk_fma_f32 v[176:177], v[242:243], v[242:243], v[176:177]
	v_and_b32_e32 v243, 0xffff0000, v91
	v_and_b32_e32 v242, 0xffff0000, v90
	v_pk_fma_f32 v[176:177], v[242:243], v[242:243], v[176:177]
	v_and_b32_e32 v243, 0xffff0000, v93
	v_and_b32_e32 v242, 0xffff0000, v92
	v_pk_fma_f32 v[176:177], v[242:243], v[242:243], v[176:177]
	v_and_b32_e32 v243, 0xffff0000, v87
	v_and_b32_e32 v242, 0xffff0000, v86
	v_pk_fma_f32 v[176:177], v[242:243], v[242:243], v[176:177]
	v_and_b32_e32 v243, 0xffff0000, v89
	v_and_b32_e32 v242, 0xffff0000, v88
	v_pk_fma_f32 v[176:177], v[242:243], v[242:243], v[176:177]
	v_and_b32_e32 v243, 0xffff0000, v83
	v_and_b32_e32 v242, 0xffff0000, v82
	v_pk_fma_f32 v[176:177], v[242:243], v[242:243], v[176:177]
	v_lshlrev_b32_e32 v243, 16, v85
	v_lshlrev_b32_e32 v242, 16, v84
	v_lshlrev_b32_e32 v246, 16, v78
	v_lshlrev_b32_e32 v247, 16, v79
	v_pk_fma_f32 v[174:175], v[242:243], v[242:243], v[174:175]
	v_lshlrev_b32_e32 v243, 16, v81
	v_pk_fma_f32 v[174:175], v[246:247], v[246:247], v[174:175]
	v_lshlrev_b32_e32 v242, 16, v80
	v_pk_fma_f32 v[174:175], v[242:243], v[242:243], v[174:175]
	v_lshlrev_b32_e32 v243, 16, v75
	v_lshlrev_b32_e32 v242, 16, v74
	v_pk_fma_f32 v[174:175], v[242:243], v[242:243], v[174:175]
	v_lshlrev_b32_e32 v243, 16, v77
	v_lshlrev_b32_e32 v242, 16, v76
	v_pk_fma_f32 v[174:175], v[242:243], v[242:243], v[174:175]
	v_lshlrev_b32_e32 v243, 16, v71
	v_lshlrev_b32_e32 v242, 16, v70
	v_pk_fma_f32 v[174:175], v[242:243], v[242:243], v[174:175]
	v_lshlrev_b32_e32 v243, 16, v73
	v_lshlrev_b32_e32 v242, 16, v72
	v_pk_fma_f32 v[174:175], v[242:243], v[242:243], v[174:175]
	v_lshlrev_b32_e32 v243, 16, v67
	v_lshlrev_b32_e32 v242, 16, v66
	v_pk_fma_f32 v[174:175], v[242:243], v[242:243], v[174:175]
	v_lshlrev_b32_e32 v243, 16, v69
	v_lshlrev_b32_e32 v242, 16, v68
	v_and_b32_e32 v245, 0xffff0000, v85
	v_and_b32_e32 v244, 0xffff0000, v84
	v_pk_fma_f32 v[174:175], v[242:243], v[242:243], v[174:175]
	v_lshlrev_b32_e32 v243, 16, v63
	v_lshlrev_b32_e32 v242, 16, v62
	v_and_b32_e32 v248, 0xffff0000, v78
	v_and_b32_e32 v249, 0xffff0000, v79
	v_pk_fma_f32 v[174:175], v[242:243], v[242:243], v[174:175]
	v_lshlrev_b32_e32 v243, 16, v65
	v_lshlrev_b32_e32 v242, 16, v64
	v_pk_fma_f32 v[176:177], v[244:245], v[244:245], v[176:177]
	v_pk_fma_f32 v[174:175], v[242:243], v[242:243], v[174:175]
	v_pk_fma_f32 v[176:177], v[248:249], v[248:249], v[176:177]
	v_and_b32_e32 v243, 0xffff0000, v81
	v_and_b32_e32 v242, 0xffff0000, v80
	v_pk_fma_f32 v[176:177], v[242:243], v[242:243], v[176:177]
	v_and_b32_e32 v243, 0xffff0000, v75
	v_and_b32_e32 v242, 0xffff0000, v74
	v_pk_fma_f32 v[176:177], v[242:243], v[242:243], v[176:177]
	v_and_b32_e32 v243, 0xffff0000, v77
	v_and_b32_e32 v242, 0xffff0000, v76
	v_pk_fma_f32 v[176:177], v[242:243], v[242:243], v[176:177]
	v_and_b32_e32 v243, 0xffff0000, v71
	v_and_b32_e32 v242, 0xffff0000, v70
	v_pk_fma_f32 v[176:177], v[242:243], v[242:243], v[176:177]
	v_and_b32_e32 v243, 0xffff0000, v73
	v_and_b32_e32 v242, 0xffff0000, v72
	v_pk_fma_f32 v[176:177], v[242:243], v[242:243], v[176:177]
	v_and_b32_e32 v243, 0xffff0000, v67
	v_and_b32_e32 v242, 0xffff0000, v66
	v_pk_fma_f32 v[176:177], v[242:243], v[242:243], v[176:177]
	v_and_b32_e32 v243, 0xffff0000, v69
	v_and_b32_e32 v242, 0xffff0000, v68
	v_pk_fma_f32 v[176:177], v[242:243], v[242:243], v[176:177]
	v_and_b32_e32 v243, 0xffff0000, v63
	v_and_b32_e32 v242, 0xffff0000, v62
	v_pk_fma_f32 v[176:177], v[242:243], v[242:243], v[176:177]
	v_and_b32_e32 v243, 0xffff0000, v65
	v_and_b32_e32 v242, 0xffff0000, v64
	v_pk_fma_f32 v[176:177], v[242:243], v[242:243], v[176:177]
	v_lshlrev_b32_e32 v243, 16, v59
	v_lshlrev_b32_e32 v242, 16, v58
	v_lshlrev_b32_e32 v246, 16, v60
	v_lshlrev_b32_e32 v247, 16, v61
	v_pk_fma_f32 v[174:175], v[242:243], v[242:243], v[174:175]
	v_lshlrev_b32_e32 v243, 16, v39
	v_pk_fma_f32 v[174:175], v[246:247], v[246:247], v[174:175]
	v_lshlrev_b32_e32 v242, 16, v38
	v_pk_fma_f32 v[174:175], v[242:243], v[242:243], v[174:175]
	v_lshlrev_b32_e32 v243, 16, v41
	v_lshlrev_b32_e32 v242, 16, v40
	v_pk_fma_f32 v[174:175], v[242:243], v[242:243], v[174:175]
	v_lshlrev_b32_e32 v243, 16, v35
	v_lshlrev_b32_e32 v242, 16, v34
	v_pk_fma_f32 v[174:175], v[242:243], v[242:243], v[174:175]
	v_lshlrev_b32_e32 v243, 16, v37
	v_lshlrev_b32_e32 v242, 16, v36
	v_pk_fma_f32 v[174:175], v[242:243], v[242:243], v[174:175]
	v_lshlrev_b32_e32 v243, 16, v31
	v_lshlrev_b32_e32 v242, 16, v30
	v_pk_fma_f32 v[174:175], v[242:243], v[242:243], v[174:175]
	v_lshlrev_b32_e32 v243, 16, v33
	v_lshlrev_b32_e32 v242, 16, v32
	v_pk_fma_f32 v[174:175], v[242:243], v[242:243], v[174:175]
	v_lshlrev_b32_e32 v243, 16, v27
	v_lshlrev_b32_e32 v242, 16, v26
	v_and_b32_e32 v245, 0xffff0000, v59
	v_and_b32_e32 v244, 0xffff0000, v58
	v_pk_fma_f32 v[174:175], v[242:243], v[242:243], v[174:175]
	v_lshlrev_b32_e32 v243, 16, v29
	v_lshlrev_b32_e32 v242, 16, v28
	v_and_b32_e32 v248, 0xffff0000, v60
	v_and_b32_e32 v249, 0xffff0000, v61
	v_pk_fma_f32 v[174:175], v[242:243], v[242:243], v[174:175]
	v_lshlrev_b32_e32 v243, 16, v23
	v_lshlrev_b32_e32 v242, 16, v22
	v_pk_fma_f32 v[176:177], v[244:245], v[244:245], v[176:177]
	v_pk_fma_f32 v[174:175], v[242:243], v[242:243], v[174:175]
	v_pk_fma_f32 v[176:177], v[248:249], v[248:249], v[176:177]
	v_and_b32_e32 v243, 0xffff0000, v39
	v_and_b32_e32 v242, 0xffff0000, v38
	v_pk_fma_f32 v[176:177], v[242:243], v[242:243], v[176:177]
	v_and_b32_e32 v243, 0xffff0000, v41
	v_and_b32_e32 v242, 0xffff0000, v40
	v_pk_fma_f32 v[176:177], v[242:243], v[242:243], v[176:177]
	v_and_b32_e32 v243, 0xffff0000, v35
	v_and_b32_e32 v242, 0xffff0000, v34
	v_pk_fma_f32 v[176:177], v[242:243], v[242:243], v[176:177]
	v_and_b32_e32 v243, 0xffff0000, v37
	v_and_b32_e32 v242, 0xffff0000, v36
	v_pk_fma_f32 v[176:177], v[242:243], v[242:243], v[176:177]
	v_and_b32_e32 v243, 0xffff0000, v31
	v_and_b32_e32 v242, 0xffff0000, v30
	v_pk_fma_f32 v[176:177], v[242:243], v[242:243], v[176:177]
	v_and_b32_e32 v243, 0xffff0000, v33
	v_and_b32_e32 v242, 0xffff0000, v32
	v_pk_fma_f32 v[176:177], v[242:243], v[242:243], v[176:177]
	v_and_b32_e32 v243, 0xffff0000, v27
	v_and_b32_e32 v242, 0xffff0000, v26
	v_pk_fma_f32 v[176:177], v[242:243], v[242:243], v[176:177]
	v_and_b32_e32 v243, 0xffff0000, v29
	v_and_b32_e32 v242, 0xffff0000, v28
	v_pk_fma_f32 v[176:177], v[242:243], v[242:243], v[176:177]
	v_and_b32_e32 v243, 0xffff0000, v23
	v_and_b32_e32 v242, 0xffff0000, v22
	v_pk_fma_f32 v[176:177], v[242:243], v[242:243], v[176:177]
	v_lshlrev_b32_e32 v243, 16, v25
	v_lshlrev_b32_e32 v242, 16, v24
	v_and_b32_e32 v245, 0xffff0000, v25
	v_and_b32_e32 v244, 0xffff0000, v24
	v_lshlrev_b32_e32 v246, 16, v18
	v_lshlrev_b32_e32 v247, 16, v19
	v_pk_fma_f32 v[174:175], v[242:243], v[242:243], v[174:175]
	v_and_b32_e32 v248, 0xffff0000, v18
	v_and_b32_e32 v249, 0xffff0000, v19
	v_pk_fma_f32 v[176:177], v[244:245], v[244:245], v[176:177]
	v_pk_fma_f32 v[174:175], v[246:247], v[246:247], v[174:175]
	v_lshlrev_b32_e32 v243, 16, v21
	v_lshlrev_b32_e32 v242, 16, v20
	v_pk_fma_f32 v[176:177], v[248:249], v[248:249], v[176:177]
	v_pk_fma_f32 v[174:175], v[242:243], v[242:243], v[174:175]
	v_and_b32_e32 v243, 0xffff0000, v21
	v_and_b32_e32 v242, 0xffff0000, v20
	v_pk_fma_f32 v[176:177], v[242:243], v[242:243], v[176:177]
	v_lshlrev_b32_e32 v243, 16, v15
	v_lshlrev_b32_e32 v242, 16, v14
	v_pk_fma_f32 v[174:175], v[242:243], v[242:243], v[174:175]
	v_and_b32_e32 v243, 0xffff0000, v15
	v_and_b32_e32 v242, 0xffff0000, v14
	v_pk_fma_f32 v[176:177], v[242:243], v[242:243], v[176:177]
	v_lshlrev_b32_e32 v243, 16, v17
	v_lshlrev_b32_e32 v242, 16, v16
	v_pk_fma_f32 v[174:175], v[242:243], v[242:243], v[174:175]
	v_and_b32_e32 v243, 0xffff0000, v17
	v_and_b32_e32 v242, 0xffff0000, v16
	v_pk_fma_f32 v[176:177], v[242:243], v[242:243], v[176:177]
	v_lshlrev_b32_e32 v243, 16, v11
	v_lshlrev_b32_e32 v242, 16, v10
	v_pk_fma_f32 v[174:175], v[242:243], v[242:243], v[174:175]
	v_and_b32_e32 v243, 0xffff0000, v11
	v_and_b32_e32 v242, 0xffff0000, v10
	v_pk_fma_f32 v[176:177], v[242:243], v[242:243], v[176:177]
	v_lshlrev_b32_e32 v243, 16, v13
	v_lshlrev_b32_e32 v242, 16, v12
	v_pk_fma_f32 v[174:175], v[242:243], v[242:243], v[174:175]
	v_and_b32_e32 v243, 0xffff0000, v13
	v_and_b32_e32 v242, 0xffff0000, v12
	v_pk_fma_f32 v[176:177], v[242:243], v[242:243], v[176:177]
	v_lshlrev_b32_e32 v243, 16, v7
	v_lshlrev_b32_e32 v242, 16, v6
	v_pk_fma_f32 v[174:175], v[242:243], v[242:243], v[174:175]
	v_and_b32_e32 v243, 0xffff0000, v7
	v_and_b32_e32 v242, 0xffff0000, v6
	v_pk_fma_f32 v[176:177], v[242:243], v[242:243], v[176:177]
	v_lshlrev_b32_e32 v243, 16, v9
	v_lshlrev_b32_e32 v242, 16, v8
	v_pk_fma_f32 v[174:175], v[242:243], v[242:243], v[174:175]
	v_and_b32_e32 v243, 0xffff0000, v9
	v_and_b32_e32 v242, 0xffff0000, v8
	v_pk_fma_f32 v[176:177], v[242:243], v[242:243], v[176:177]
	v_lshlrev_b32_e32 v243, 16, v3
	v_lshlrev_b32_e32 v242, 16, v2
	v_pk_fma_f32 v[174:175], v[242:243], v[242:243], v[174:175]
	v_and_b32_e32 v243, 0xffff0000, v3
	v_and_b32_e32 v242, 0xffff0000, v2
	v_pk_fma_f32 v[176:177], v[242:243], v[242:243], v[176:177]
	v_lshlrev_b32_e32 v243, 16, v5
	v_lshlrev_b32_e32 v242, 16, v4
	v_pk_fma_f32 v[174:175], v[242:243], v[242:243], v[174:175]
	v_and_b32_e32 v243, 0xffff0000, v5
	v_and_b32_e32 v242, 0xffff0000, v4
	v_pk_fma_f32 v[176:177], v[242:243], v[242:243], v[176:177]
	s_mov_b32 s2, 0xf800000
	v_pk_add_f32 v[174:175], v[176:177], v[174:175]
	s_waitcnt lgkmcnt(3)
	v_mfma_f32_16x16x32_bf16 v[118:121], v[2:5], v[158:161], v[118:121]
	v_add_f32_e32 v163, v175, v174
	ds_bpermute_b32 v174, v171, v163
	ds_read_b128 v[242:245], v170
	s_waitcnt lgkmcnt(1)
	v_add_f32_e32 v163, v163, v174
	ds_bpermute_b32 v174, v172, v163
	s_waitcnt lgkmcnt(0)
	v_add_f32_e32 v163, v163, v174
	v_fmamk_f32 v163, v163, 0x3a800000, v236
	v_mul_f32_e32 v174, 0x4f800000, v163
	v_cmp_gt_f32_e32 vcc, s2, v163
	s_nop 1
	v_cndmask_b32_e32 v163, v163, v174, vcc
	v_sqrt_f32_e32 v174, v163
	s_nop 0
	v_add_u32_e32 v175, -1, v174
	v_fma_f32 v176, -v175, v174, v163
	v_cmp_ge_f32_e64 s[2:3], 0, v176
	v_add_u32_e32 v176, 1, v174
	s_nop 0
	v_cndmask_b32_e64 v175, v174, v175, s[2:3]
	v_fma_f32 v174, -v176, v174, v163
	v_cmp_lt_f32_e64 s[2:3], 0, v174
	s_nop 1
	v_cndmask_b32_e64 v174, v175, v176, s[2:3]
	v_mul_f32_e32 v175, 0x37800000, v174
	v_cndmask_b32_e32 v174, v174, v175, vcc
	v_cmp_class_f32_e32 vcc, v163, v237
	s_nop 1
	v_cndmask_b32_e32 v163, v174, v163, vcc
	v_div_scale_f32 v174, s[2:3], v163, v163, 1.0
	v_rcp_f32_e32 v175, v174
	s_nop 0
	v_fma_f32 v158, -v174, v175, 1.0
	v_fmac_f32_e32 v175, v158, v175
	v_div_scale_f32 v158, vcc, 1.0, v163, 1.0
	v_mul_f32_e32 v159, v158, v175
	v_fma_f32 v160, -v174, v159, v158
	v_fmac_f32_e32 v159, v160, v175
	v_fma_f32 v158, -v174, v159, v158
	v_div_fmas_f32 v158, v158, v175, v159
	ds_read_b128 v[246:249], v170 offset:16
	ds_read_b128 v[250:253], v170 offset:32
	ds_read_b128 v[174:177], v170 offset:48
	v_div_fixup_f32 v158, v158, v163, 1.0
	v_pk_mul_f32 v[160:161], v[244:245], v[158:159] op_sel_hi:[1,0]
	v_pk_mul_f32 v[242:243], v[242:243], v[158:159] op_sel_hi:[1,0]
	s_waitcnt lgkmcnt(2)
	v_pk_mul_f32 v[244:245], v[248:249], v[158:159] op_sel_hi:[1,0]
	v_pk_mul_f32 v[246:247], v[246:247], v[158:159] op_sel_hi:[1,0]
	s_waitcnt lgkmcnt(1)
	v_pk_mul_f32 v[248:249], v[252:253], v[158:159] op_sel_hi:[1,0]
	v_pk_mul_f32 v[250:251], v[250:251], v[158:159] op_sel_hi:[1,0]
	s_waitcnt lgkmcnt(0)
	v_pk_mul_f32 v[176:177], v[176:177], v[158:159] op_sel_hi:[1,0]
	v_pk_mul_f32 v[174:175], v[174:175], v[158:159] op_sel_hi:[1,0]
	v_lshlrev_b32_e32 v159, 16, v146
	v_and_b32_e32 v146, 0xffff0000, v146
	v_mul_f32_e32 v159, v242, v159
	v_mul_f32_e32 v146, v243, v146
	v_lshlrev_b32_e32 v163, 16, v147
	v_mul_f32_e32 v160, v160, v163
	v_med3_f32 v159, v159, s85, v240
	v_med3_f32 v163, v146, s85, v240
	v_mov_b32_e32 v146, 0
	v_cvt_pk_fp8_f32 v146, v159, v163
	v_and_b32_e32 v147, 0xffff0000, v147
	v_mul_f32_e32 v147, v161, v147
	v_med3_f32 v159, v160, s85, v240
	v_med3_f32 v147, v147, s85, v240
	v_cvt_pk_fp8_f32 v146, v159, v147 op_sel:[0,0,1]
	v_lshlrev_b32_e32 v147, 16, v148
	v_and_b32_e32 v148, 0xffff0000, v148
	v_mul_f32_e32 v147, v246, v147
	v_mul_f32_e32 v148, v247, v148
	v_med3_f32 v160, v147, s85, v240
	v_med3_f32 v148, v148, s85, v240
	v_mov_b32_e32 v147, 0
	v_cvt_pk_fp8_f32 v147, v160, v148
	v_lshlrev_b32_e32 v159, 16, v149
	v_and_b32_e32 v149, 0xffff0000, v149
	v_mul_f32_e32 v159, v244, v159
	v_mul_f32_e32 v148, v245, v149
	v_med3_f32 v149, v159, s85, v240
	v_med3_f32 v148, v148, s85, v240
	v_cvt_pk_fp8_f32 v147, v149, v148 op_sel:[0,0,1]
	v_lshlrev_b32_e32 v148, 16, v130
	v_and_b32_e32 v130, 0xffff0000, v130
	v_mul_f32_e32 v148, v250, v148
	v_mul_f32_e32 v130, v251, v130
	v_med3_f32 v159, v148, s85, v240
	v_med3_f32 v130, v130, s85, v240
	v_mov_b32_e32 v148, 0
	v_cvt_pk_fp8_f32 v148, v159, v130
	v_lshlrev_b32_e32 v149, 16, v131
	v_and_b32_e32 v131, 0xffff0000, v131
	v_mul_f32_e32 v149, v248, v149
	v_mul_f32_e32 v130, v249, v131
	v_med3_f32 v131, v149, s85, v240
	v_med3_f32 v130, v130, s85, v240
	v_cvt_pk_fp8_f32 v148, v131, v130 op_sel:[0,0,1]
	v_lshlrev_b32_e32 v130, 16, v132
	v_and_b32_e32 v131, 0xffff0000, v132
	v_mul_f32_e32 v130, v174, v130
	v_mul_f32_e32 v131, v175, v131
	v_med3_f32 v130, v130, s85, v240
	v_med3_f32 v131, v131, s85, v240
	v_mov_b32_e32 v149, 0
	v_cvt_pk_fp8_f32 v149, v130, v131
	v_lshlrev_b32_e32 v132, 16, v133
	v_and_b32_e32 v133, 0xffff0000, v133
	v_mul_f32_e32 v132, v176, v132
	v_mul_f32_e32 v130, v177, v133
	v_med3_f32 v131, v132, s85, v240
	v_med3_f32 v130, v130, s85, v240
	v_cvt_pk_fp8_f32 v149, v131, v130 op_sel:[0,0,1]
	v_mfma_f32_16x16x32_bf16 v[130:133], v[2:5], v[154:157], v[150:153]
	global_store_dwordx4 v[164:165], v[146:149], off offset:-512
	ds_read_b128 v[146:149], v170 offset:256
	s_nop 0
	ds_read_b128 v[150:153], v170 offset:272
	ds_read_b128 v[154:157], v170 offset:288
	ds_read_b128 v[174:177], v170 offset:304
	s_waitcnt lgkmcnt(3)
	v_pk_mul_f32 v[148:149], v[158:159], v[148:149] op_sel_hi:[0,1]
	v_pk_mul_f32 v[146:147], v[158:159], v[146:147] op_sel_hi:[0,1]
	s_waitcnt lgkmcnt(2)
	v_pk_mul_f32 v[152:153], v[158:159], v[152:153] op_sel_hi:[0,1]
	v_pk_mul_f32 v[150:151], v[158:159], v[150:151] op_sel_hi:[0,1]
	s_waitcnt lgkmcnt(1)
	v_pk_mul_f32 v[156:157], v[158:159], v[156:157] op_sel_hi:[0,1]
	v_pk_mul_f32 v[154:155], v[158:159], v[154:155] op_sel_hi:[0,1]
	s_waitcnt lgkmcnt(0)
	v_pk_mul_f32 v[160:161], v[158:159], v[176:177] op_sel_hi:[0,1]
	v_pk_mul_f32 v[174:175], v[158:159], v[174:175] op_sel_hi:[0,1]
	v_lshlrev_b32_e32 v159, 16, v142
	v_and_b32_e32 v142, 0xffff0000, v142
	v_mul_f32_e32 v146, v146, v159
	v_mul_f32_e32 v142, v147, v142
	v_lshlrev_b32_e32 v147, 16, v143
	v_mul_f32_e32 v147, v148, v147
	v_med3_f32 v146, v146, s85, v240
	v_med3_f32 v148, v142, s85, v240
	v_mov_b32_e32 v142, 0
	v_cvt_pk_fp8_f32 v142, v146, v148
	v_and_b32_e32 v143, 0xffff0000, v143
	v_mul_f32_e32 v143, v149, v143
	v_med3_f32 v146, v147, s85, v240
	v_med3_f32 v143, v143, s85, v240
	v_cvt_pk_fp8_f32 v142, v146, v143 op_sel:[0,0,1]
	v_lshlrev_b32_e32 v143, 16, v144
	v_and_b32_e32 v144, 0xffff0000, v144
	v_mul_f32_e32 v143, v150, v143
	v_mul_f32_e32 v144, v151, v144
	v_med3_f32 v147, v143, s85, v240
	v_med3_f32 v144, v144, s85, v240
	v_mov_b32_e32 v143, 0
	v_cvt_pk_fp8_f32 v143, v147, v144
	v_lshlrev_b32_e32 v146, 16, v145
	v_and_b32_e32 v145, 0xffff0000, v145
	v_mul_f32_e32 v146, v152, v146
	v_mul_f32_e32 v144, v153, v145
	v_med3_f32 v145, v146, s85, v240
	v_med3_f32 v144, v144, s85, v240
	v_cvt_pk_fp8_f32 v143, v145, v144 op_sel:[0,0,1]
	v_lshlrev_b32_e32 v144, 16, v138
	v_and_b32_e32 v138, 0xffff0000, v138
	v_mul_f32_e32 v144, v154, v144
	v_mul_f32_e32 v138, v155, v138
	v_med3_f32 v146, v144, s85, v240
	v_med3_f32 v138, v138, s85, v240
	v_mov_b32_e32 v144, 0
	v_cvt_pk_fp8_f32 v144, v146, v138
	v_lshlrev_b32_e32 v145, 16, v139
	v_and_b32_e32 v139, 0xffff0000, v139
	v_mul_f32_e32 v145, v156, v145
	v_mul_f32_e32 v138, v157, v139
	v_med3_f32 v139, v145, s85, v240
	v_med3_f32 v138, v138, s85, v240
	v_cvt_pk_fp8_f32 v144, v139, v138 op_sel:[0,0,1]
	v_lshlrev_b32_e32 v138, 16, v140
	v_and_b32_e32 v139, 0xffff0000, v140
	v_mul_f32_e32 v138, v174, v138
	v_mul_f32_e32 v139, v175, v139
	v_med3_f32 v138, v138, s85, v240
	v_med3_f32 v139, v139, s85, v240
	v_mov_b32_e32 v145, 0
	v_cvt_pk_fp8_f32 v145, v138, v139
	v_lshlrev_b32_e32 v140, 16, v141
	v_and_b32_e32 v141, 0xffff0000, v141
	v_mul_f32_e32 v140, v160, v140
	v_mul_f32_e32 v138, v161, v141
	v_med3_f32 v139, v140, s85, v240
	v_med3_f32 v138, v138, s85, v240
	v_cvt_pk_fp8_f32 v145, v139, v138 op_sel:[0,0,1]
	global_store_dwordx4 v[164:165], v[142:145], off offset:-448
	ds_read_b128 v[138:141], v170 offset:512
	ds_read_b128 v[142:145], v170 offset:528
	ds_read_b128 v[146:149], v170 offset:544
	ds_read_b128 v[150:153], v170 offset:560
	v_lshlrev_b32_e32 v154, 16, v134
	s_waitcnt lgkmcnt(3)
	v_pk_mul_f32 v[138:139], v[158:159], v[138:139] op_sel_hi:[0,1]
	v_and_b32_e32 v134, 0xffff0000, v134
	v_pk_mul_f32 v[140:141], v[158:159], v[140:141] op_sel_hi:[0,1]
	v_mul_f32_e32 v138, v138, v154
	v_mul_f32_e32 v134, v139, v134
	v_lshlrev_b32_e32 v139, 16, v135
	v_mul_f32_e32 v139, v140, v139
	v_med3_f32 v138, v138, s85, v240
	v_med3_f32 v140, v134, s85, v240
	v_mov_b32_e32 v134, 0
	v_cvt_pk_fp8_f32 v134, v138, v140
	v_and_b32_e32 v135, 0xffff0000, v135
	v_mul_f32_e32 v135, v141, v135
	v_med3_f32 v138, v139, s85, v240
	v_med3_f32 v135, v135, s85, v240
	s_waitcnt lgkmcnt(2)
	v_pk_mul_f32 v[142:143], v[158:159], v[142:143] op_sel_hi:[0,1]
	v_cvt_pk_fp8_f32 v134, v138, v135 op_sel:[0,0,1]
	v_lshlrev_b32_e32 v135, 16, v136
	v_and_b32_e32 v136, 0xffff0000, v136
	v_mul_f32_e32 v135, v142, v135
	v_mul_f32_e32 v136, v143, v136
	v_med3_f32 v139, v135, s85, v240
	v_med3_f32 v136, v136, s85, v240
	v_mov_b32_e32 v135, 0
	v_cvt_pk_fp8_f32 v135, v139, v136
	v_pk_mul_f32 v[144:145], v[158:159], v[144:145] op_sel_hi:[0,1]
	v_lshlrev_b32_e32 v138, 16, v137
	v_and_b32_e32 v137, 0xffff0000, v137
	v_mul_f32_e32 v138, v144, v138
	v_mul_f32_e32 v136, v145, v137
	v_med3_f32 v137, v138, s85, v240
	v_med3_f32 v136, v136, s85, v240
	s_waitcnt lgkmcnt(1)
	v_pk_mul_f32 v[146:147], v[158:159], v[146:147] op_sel_hi:[0,1]
	v_cvt_pk_fp8_f32 v135, v137, v136 op_sel:[0,0,1]
	v_lshlrev_b32_e32 v136, 16, v126
	v_and_b32_e32 v126, 0xffff0000, v126
	v_mul_f32_e32 v136, v146, v136
	v_mul_f32_e32 v126, v147, v126
	v_med3_f32 v138, v136, s85, v240
	v_med3_f32 v126, v126, s85, v240
	v_mov_b32_e32 v136, 0
	v_cvt_pk_fp8_f32 v136, v138, v126
	v_pk_mul_f32 v[148:149], v[158:159], v[148:149] op_sel_hi:[0,1]
	v_lshlrev_b32_e32 v137, 16, v127
	v_and_b32_e32 v127, 0xffff0000, v127
	v_mul_f32_e32 v137, v148, v137
	v_mul_f32_e32 v126, v149, v127
	v_med3_f32 v127, v137, s85, v240
	v_med3_f32 v126, v126, s85, v240
	s_waitcnt lgkmcnt(0)
	v_pk_mul_f32 v[150:151], v[158:159], v[150:151] op_sel_hi:[0,1]
	v_cvt_pk_fp8_f32 v136, v127, v126 op_sel:[0,0,1]
	v_lshlrev_b32_e32 v126, 16, v128
	v_and_b32_e32 v127, 0xffff0000, v128
	v_mul_f32_e32 v126, v150, v126
	v_mul_f32_e32 v127, v151, v127
	v_med3_f32 v126, v126, s85, v240
	v_med3_f32 v127, v127, s85, v240
	v_mov_b32_e32 v137, 0
	v_cvt_pk_fp8_f32 v137, v126, v127
	v_pk_mul_f32 v[152:153], v[158:159], v[152:153] op_sel_hi:[0,1]
	v_lshlrev_b32_e32 v128, 16, v129
	v_and_b32_e32 v129, 0xffff0000, v129
	v_mul_f32_e32 v128, v152, v128
	v_mul_f32_e32 v126, v153, v129
	v_med3_f32 v127, v128, s85, v240
	v_med3_f32 v126, v126, s85, v240
	v_cvt_pk_fp8_f32 v137, v127, v126 op_sel:[0,0,1]
	global_store_dwordx4 v[164:165], v[134:137], off offset:-384
	ds_read_b128 v[126:129], v170 offset:768
	ds_read_b128 v[134:137], v170 offset:784
	ds_read_b128 v[138:141], v170 offset:800
	ds_read_b128 v[142:145], v170 offset:816
	v_lshlrev_b32_e32 v146, 16, v122
	s_waitcnt lgkmcnt(3)
	v_pk_mul_f32 v[126:127], v[158:159], v[126:127] op_sel_hi:[0,1]
	v_and_b32_e32 v122, 0xffff0000, v122
	v_pk_mul_f32 v[128:129], v[158:159], v[128:129] op_sel_hi:[0,1]
	v_mul_f32_e32 v126, v126, v146
	v_mul_f32_e32 v122, v127, v122
	v_lshlrev_b32_e32 v127, 16, v123
	v_mul_f32_e32 v127, v128, v127
	v_med3_f32 v126, v126, s85, v240
	v_med3_f32 v128, v122, s85, v240
	v_mov_b32_e32 v122, 0
	v_cvt_pk_fp8_f32 v122, v126, v128
	v_and_b32_e32 v123, 0xffff0000, v123
	v_mul_f32_e32 v123, v129, v123
	v_med3_f32 v126, v127, s85, v240
	v_med3_f32 v123, v123, s85, v240
	s_waitcnt lgkmcnt(2)
	v_pk_mul_f32 v[134:135], v[158:159], v[134:135] op_sel_hi:[0,1]
	v_cvt_pk_fp8_f32 v122, v126, v123 op_sel:[0,0,1]
	v_lshlrev_b32_e32 v123, 16, v124
	v_and_b32_e32 v124, 0xffff0000, v124
	v_mul_f32_e32 v123, v134, v123
	v_mul_f32_e32 v124, v135, v124
	v_med3_f32 v127, v123, s85, v240
	v_med3_f32 v124, v124, s85, v240
	v_mov_b32_e32 v123, 0
	v_cvt_pk_fp8_f32 v123, v127, v124
	v_pk_mul_f32 v[136:137], v[158:159], v[136:137] op_sel_hi:[0,1]
	v_lshlrev_b32_e32 v126, 16, v125
	v_and_b32_e32 v125, 0xffff0000, v125
	v_mul_f32_e32 v126, v136, v126
	v_mul_f32_e32 v124, v137, v125
	v_med3_f32 v125, v126, s85, v240
	v_med3_f32 v124, v124, s85, v240
	s_waitcnt lgkmcnt(1)
	v_pk_mul_f32 v[138:139], v[158:159], v[138:139] op_sel_hi:[0,1]
	v_cvt_pk_fp8_f32 v123, v125, v124 op_sel:[0,0,1]
	v_lshlrev_b32_e32 v124, 16, v114
	v_and_b32_e32 v114, 0xffff0000, v114
	v_mul_f32_e32 v124, v138, v124
	v_mul_f32_e32 v114, v139, v114
	v_med3_f32 v126, v124, s85, v240
	v_med3_f32 v114, v114, s85, v240
	v_mov_b32_e32 v124, 0
	v_cvt_pk_fp8_f32 v124, v126, v114
	v_pk_mul_f32 v[140:141], v[158:159], v[140:141] op_sel_hi:[0,1]
	v_lshlrev_b32_e32 v125, 16, v115
	v_and_b32_e32 v115, 0xffff0000, v115
	v_mul_f32_e32 v125, v140, v125
	v_mul_f32_e32 v114, v141, v115
	v_med3_f32 v115, v125, s85, v240
	v_med3_f32 v114, v114, s85, v240
	s_waitcnt lgkmcnt(0)
	v_pk_mul_f32 v[142:143], v[158:159], v[142:143] op_sel_hi:[0,1]
	v_cvt_pk_fp8_f32 v124, v115, v114 op_sel:[0,0,1]
	v_lshlrev_b32_e32 v114, 16, v116
	v_and_b32_e32 v115, 0xffff0000, v116
	v_mul_f32_e32 v114, v142, v114
	v_mul_f32_e32 v115, v143, v115
	v_med3_f32 v114, v114, s85, v240
	v_med3_f32 v115, v115, s85, v240
	v_mov_b32_e32 v125, 0
	v_cvt_pk_fp8_f32 v125, v114, v115
	v_pk_mul_f32 v[144:145], v[158:159], v[144:145] op_sel_hi:[0,1]
	v_lshlrev_b32_e32 v116, 16, v117
	v_and_b32_e32 v117, 0xffff0000, v117
	v_mul_f32_e32 v116, v144, v116
	v_mul_f32_e32 v114, v145, v117
	v_med3_f32 v115, v116, s85, v240
	v_med3_f32 v114, v114, s85, v240
	v_cvt_pk_fp8_f32 v125, v115, v114 op_sel:[0,0,1]
	global_store_dwordx4 v[164:165], v[122:125], off offset:-320
	ds_read_b128 v[114:117], v170 offset:1024
	ds_read_b128 v[122:125], v170 offset:1040
	ds_read_b128 v[126:129], v170 offset:1056
	ds_read_b128 v[134:137], v170 offset:1072
	v_lshlrev_b32_e32 v138, 16, v110
	s_waitcnt lgkmcnt(3)
	v_pk_mul_f32 v[114:115], v[158:159], v[114:115] op_sel_hi:[0,1]
	v_and_b32_e32 v110, 0xffff0000, v110
	v_pk_mul_f32 v[116:117], v[158:159], v[116:117] op_sel_hi:[0,1]
	v_mul_f32_e32 v114, v114, v138
	v_mul_f32_e32 v110, v115, v110
	v_lshlrev_b32_e32 v115, 16, v111
	v_mul_f32_e32 v115, v116, v115
	v_med3_f32 v114, v114, s85, v240
	v_med3_f32 v116, v110, s85, v240
	v_mov_b32_e32 v110, 0
	v_cvt_pk_fp8_f32 v110, v114, v116
	v_and_b32_e32 v111, 0xffff0000, v111
	v_mul_f32_e32 v111, v117, v111
	v_med3_f32 v114, v115, s85, v240
	v_med3_f32 v111, v111, s85, v240
	s_waitcnt lgkmcnt(2)
	v_pk_mul_f32 v[122:123], v[158:159], v[122:123] op_sel_hi:[0,1]
	v_cvt_pk_fp8_f32 v110, v114, v111 op_sel:[0,0,1]
	v_lshlrev_b32_e32 v111, 16, v112
	v_and_b32_e32 v112, 0xffff0000, v112
	v_mul_f32_e32 v111, v122, v111
	v_mul_f32_e32 v112, v123, v112
	v_med3_f32 v115, v111, s85, v240
	v_med3_f32 v112, v112, s85, v240
	v_mov_b32_e32 v111, 0
	v_cvt_pk_fp8_f32 v111, v115, v112
	v_pk_mul_f32 v[124:125], v[158:159], v[124:125] op_sel_hi:[0,1]
	v_lshlrev_b32_e32 v114, 16, v113
	v_and_b32_e32 v113, 0xffff0000, v113
	v_mul_f32_e32 v114, v124, v114
	v_mul_f32_e32 v112, v125, v113
	v_med3_f32 v113, v114, s85, v240
	v_med3_f32 v112, v112, s85, v240
	s_waitcnt lgkmcnt(1)
	v_pk_mul_f32 v[126:127], v[158:159], v[126:127] op_sel_hi:[0,1]
	v_cvt_pk_fp8_f32 v111, v113, v112 op_sel:[0,0,1]
	v_lshlrev_b32_e32 v112, 16, v106
	v_and_b32_e32 v106, 0xffff0000, v106
	v_mul_f32_e32 v112, v126, v112
	v_mul_f32_e32 v106, v127, v106
	v_med3_f32 v114, v112, s85, v240
	v_med3_f32 v106, v106, s85, v240
	v_mov_b32_e32 v112, 0
	v_cvt_pk_fp8_f32 v112, v114, v106
	v_pk_mul_f32 v[128:129], v[158:159], v[128:129] op_sel_hi:[0,1]
	v_lshlrev_b32_e32 v113, 16, v107
	v_and_b32_e32 v107, 0xffff0000, v107
	v_mul_f32_e32 v113, v128, v113
	v_mul_f32_e32 v106, v129, v107
	v_med3_f32 v107, v113, s85, v240
	v_med3_f32 v106, v106, s85, v240
	s_waitcnt lgkmcnt(0)
	v_pk_mul_f32 v[134:135], v[158:159], v[134:135] op_sel_hi:[0,1]
	v_cvt_pk_fp8_f32 v112, v107, v106 op_sel:[0,0,1]
	v_lshlrev_b32_e32 v106, 16, v108
	v_and_b32_e32 v107, 0xffff0000, v108
	v_mul_f32_e32 v106, v134, v106
	v_mul_f32_e32 v107, v135, v107
	v_med3_f32 v106, v106, s85, v240
	v_med3_f32 v107, v107, s85, v240
	v_mov_b32_e32 v113, 0
	v_cvt_pk_fp8_f32 v113, v106, v107
	v_pk_mul_f32 v[136:137], v[158:159], v[136:137] op_sel_hi:[0,1]
	v_lshlrev_b32_e32 v108, 16, v109
	v_and_b32_e32 v109, 0xffff0000, v109
	v_mul_f32_e32 v108, v136, v108
	v_mul_f32_e32 v106, v137, v109
	v_med3_f32 v107, v108, s85, v240
	v_med3_f32 v106, v106, s85, v240
	v_cvt_pk_fp8_f32 v113, v107, v106 op_sel:[0,0,1]
	global_store_dwordx4 v[164:165], v[110:113], off offset:-256
	ds_read_b128 v[106:109], v170 offset:1280
	ds_read_b128 v[110:113], v170 offset:1296
	ds_read_b128 v[114:117], v170 offset:1312
	ds_read_b128 v[122:125], v170 offset:1328
	v_lshlrev_b32_e32 v126, 16, v102
	s_waitcnt lgkmcnt(3)
	v_pk_mul_f32 v[106:107], v[158:159], v[106:107] op_sel_hi:[0,1]
	v_and_b32_e32 v102, 0xffff0000, v102
	v_pk_mul_f32 v[108:109], v[158:159], v[108:109] op_sel_hi:[0,1]
	v_mul_f32_e32 v106, v106, v126
	v_mul_f32_e32 v102, v107, v102
	v_lshlrev_b32_e32 v107, 16, v103
	v_mul_f32_e32 v107, v108, v107
	v_med3_f32 v106, v106, s85, v240
	v_med3_f32 v108, v102, s85, v240
	v_mov_b32_e32 v102, 0
	v_cvt_pk_fp8_f32 v102, v106, v108
	v_and_b32_e32 v103, 0xffff0000, v103
	v_mul_f32_e32 v103, v109, v103
	v_med3_f32 v106, v107, s85, v240
	v_med3_f32 v103, v103, s85, v240
	s_waitcnt lgkmcnt(2)
	v_pk_mul_f32 v[110:111], v[158:159], v[110:111] op_sel_hi:[0,1]
	v_cvt_pk_fp8_f32 v102, v106, v103 op_sel:[0,0,1]
	v_lshlrev_b32_e32 v103, 16, v104
	v_and_b32_e32 v104, 0xffff0000, v104
	v_mul_f32_e32 v103, v110, v103
	v_mul_f32_e32 v104, v111, v104
	v_med3_f32 v107, v103, s85, v240
	v_med3_f32 v104, v104, s85, v240
	v_mov_b32_e32 v103, 0
	v_cvt_pk_fp8_f32 v103, v107, v104
	v_pk_mul_f32 v[112:113], v[158:159], v[112:113] op_sel_hi:[0,1]
	v_lshlrev_b32_e32 v106, 16, v105
	v_and_b32_e32 v105, 0xffff0000, v105
	v_mul_f32_e32 v106, v112, v106
	v_mul_f32_e32 v104, v113, v105
	v_med3_f32 v105, v106, s85, v240
	v_med3_f32 v104, v104, s85, v240
	s_waitcnt lgkmcnt(1)
	v_pk_mul_f32 v[114:115], v[158:159], v[114:115] op_sel_hi:[0,1]
	v_cvt_pk_fp8_f32 v103, v105, v104 op_sel:[0,0,1]
	v_lshlrev_b32_e32 v104, 16, v98
	v_and_b32_e32 v98, 0xffff0000, v98
	v_mul_f32_e32 v104, v114, v104
	v_mul_f32_e32 v98, v115, v98
	v_med3_f32 v106, v104, s85, v240
	v_med3_f32 v98, v98, s85, v240
	v_mov_b32_e32 v104, 0
	v_cvt_pk_fp8_f32 v104, v106, v98
	v_pk_mul_f32 v[116:117], v[158:159], v[116:117] op_sel_hi:[0,1]
	v_lshlrev_b32_e32 v105, 16, v99
	v_and_b32_e32 v99, 0xffff0000, v99
	v_mul_f32_e32 v105, v116, v105
	v_mul_f32_e32 v98, v117, v99
	v_med3_f32 v99, v105, s85, v240
	v_med3_f32 v98, v98, s85, v240
	s_waitcnt lgkmcnt(0)
	v_pk_mul_f32 v[122:123], v[158:159], v[122:123] op_sel_hi:[0,1]
	v_cvt_pk_fp8_f32 v104, v99, v98 op_sel:[0,0,1]
	v_lshlrev_b32_e32 v98, 16, v100
	v_and_b32_e32 v99, 0xffff0000, v100
	v_mul_f32_e32 v98, v122, v98
	v_mul_f32_e32 v99, v123, v99
	v_med3_f32 v98, v98, s85, v240
	v_med3_f32 v99, v99, s85, v240
	v_mov_b32_e32 v105, 0
	v_cvt_pk_fp8_f32 v105, v98, v99
	v_pk_mul_f32 v[124:125], v[158:159], v[124:125] op_sel_hi:[0,1]
	v_lshlrev_b32_e32 v100, 16, v101
	v_and_b32_e32 v101, 0xffff0000, v101
	v_mul_f32_e32 v100, v124, v100
	v_mul_f32_e32 v98, v125, v101
	v_med3_f32 v99, v100, s85, v240
	v_med3_f32 v98, v98, s85, v240
	v_cvt_pk_fp8_f32 v105, v99, v98 op_sel:[0,0,1]
	global_store_dwordx4 v[164:165], v[102:105], off offset:-192
	ds_read_b128 v[98:101], v170 offset:1536
	ds_read_b128 v[102:105], v170 offset:1552
	ds_read_b128 v[106:109], v170 offset:1568
	ds_read_b128 v[110:113], v170 offset:1584
	v_lshlrev_b32_e32 v114, 16, v94
	s_waitcnt lgkmcnt(3)
	v_pk_mul_f32 v[98:99], v[158:159], v[98:99] op_sel_hi:[0,1]
	v_and_b32_e32 v94, 0xffff0000, v94
	v_pk_mul_f32 v[100:101], v[158:159], v[100:101] op_sel_hi:[0,1]
	v_mul_f32_e32 v98, v98, v114
	v_mul_f32_e32 v94, v99, v94
	v_lshlrev_b32_e32 v99, 16, v95
	v_mul_f32_e32 v99, v100, v99
	v_med3_f32 v98, v98, s85, v240
	v_med3_f32 v100, v94, s85, v240
	v_mov_b32_e32 v94, 0
	v_cvt_pk_fp8_f32 v94, v98, v100
	v_and_b32_e32 v95, 0xffff0000, v95
	v_mul_f32_e32 v95, v101, v95
	v_med3_f32 v98, v99, s85, v240
	v_med3_f32 v95, v95, s85, v240
	s_waitcnt lgkmcnt(2)
	v_pk_mul_f32 v[102:103], v[158:159], v[102:103] op_sel_hi:[0,1]
	v_cvt_pk_fp8_f32 v94, v98, v95 op_sel:[0,0,1]
	v_lshlrev_b32_e32 v95, 16, v96
	v_and_b32_e32 v96, 0xffff0000, v96
	v_mul_f32_e32 v95, v102, v95
	v_mul_f32_e32 v96, v103, v96
	v_med3_f32 v99, v95, s85, v240
	v_med3_f32 v96, v96, s85, v240
	v_mov_b32_e32 v95, 0
	v_cvt_pk_fp8_f32 v95, v99, v96
	v_pk_mul_f32 v[104:105], v[158:159], v[104:105] op_sel_hi:[0,1]
	v_lshlrev_b32_e32 v98, 16, v97
	v_and_b32_e32 v97, 0xffff0000, v97
	v_mul_f32_e32 v98, v104, v98
	v_mul_f32_e32 v96, v105, v97
	v_med3_f32 v97, v98, s85, v240
	v_med3_f32 v96, v96, s85, v240
	s_waitcnt lgkmcnt(1)
	v_pk_mul_f32 v[106:107], v[158:159], v[106:107] op_sel_hi:[0,1]
	v_cvt_pk_fp8_f32 v95, v97, v96 op_sel:[0,0,1]
	v_lshlrev_b32_e32 v96, 16, v90
	v_and_b32_e32 v90, 0xffff0000, v90
	v_mul_f32_e32 v96, v106, v96
	v_mul_f32_e32 v90, v107, v90
	v_med3_f32 v98, v96, s85, v240
	v_med3_f32 v90, v90, s85, v240
	v_mov_b32_e32 v96, 0
	v_cvt_pk_fp8_f32 v96, v98, v90
	v_pk_mul_f32 v[108:109], v[158:159], v[108:109] op_sel_hi:[0,1]
	v_lshlrev_b32_e32 v97, 16, v91
	v_and_b32_e32 v91, 0xffff0000, v91
	v_mul_f32_e32 v97, v108, v97
	v_mul_f32_e32 v90, v109, v91
	v_med3_f32 v91, v97, s85, v240
	v_med3_f32 v90, v90, s85, v240
	s_waitcnt lgkmcnt(0)
	v_pk_mul_f32 v[110:111], v[158:159], v[110:111] op_sel_hi:[0,1]
	v_cvt_pk_fp8_f32 v96, v91, v90 op_sel:[0,0,1]
	v_lshlrev_b32_e32 v90, 16, v92
	v_and_b32_e32 v91, 0xffff0000, v92
	v_mul_f32_e32 v90, v110, v90
	v_mul_f32_e32 v91, v111, v91
	v_med3_f32 v90, v90, s85, v240
	v_med3_f32 v91, v91, s85, v240
	v_mov_b32_e32 v97, 0
	v_cvt_pk_fp8_f32 v97, v90, v91
	v_pk_mul_f32 v[112:113], v[158:159], v[112:113] op_sel_hi:[0,1]
	v_lshlrev_b32_e32 v92, 16, v93
	v_and_b32_e32 v93, 0xffff0000, v93
	v_mul_f32_e32 v92, v112, v92
	v_mul_f32_e32 v90, v113, v93
	v_med3_f32 v91, v92, s85, v240
	v_med3_f32 v90, v90, s85, v240
	v_cvt_pk_fp8_f32 v97, v91, v90 op_sel:[0,0,1]
	global_store_dwordx4 v[164:165], v[94:97], off offset:-128
	ds_read_b128 v[90:93], v170 offset:1792
	ds_read_b128 v[94:97], v170 offset:1808
	ds_read_b128 v[98:101], v170 offset:1824
	ds_read_b128 v[102:105], v170 offset:1840
	v_lshlrev_b32_e32 v106, 16, v86
	s_waitcnt lgkmcnt(3)
	v_pk_mul_f32 v[90:91], v[158:159], v[90:91] op_sel_hi:[0,1]
	v_and_b32_e32 v86, 0xffff0000, v86
	v_pk_mul_f32 v[92:93], v[158:159], v[92:93] op_sel_hi:[0,1]
	v_mul_f32_e32 v90, v90, v106
	v_mul_f32_e32 v86, v91, v86
	v_lshlrev_b32_e32 v91, 16, v87
	v_mul_f32_e32 v91, v92, v91
	v_med3_f32 v90, v90, s85, v240
	v_med3_f32 v92, v86, s85, v240
	v_mov_b32_e32 v86, 0
	v_cvt_pk_fp8_f32 v86, v90, v92
	v_and_b32_e32 v87, 0xffff0000, v87
	v_mul_f32_e32 v87, v93, v87
	v_med3_f32 v90, v91, s85, v240
	v_med3_f32 v87, v87, s85, v240
	s_waitcnt lgkmcnt(2)
	v_pk_mul_f32 v[94:95], v[158:159], v[94:95] op_sel_hi:[0,1]
	v_cvt_pk_fp8_f32 v86, v90, v87 op_sel:[0,0,1]
	v_lshlrev_b32_e32 v87, 16, v88
	v_and_b32_e32 v88, 0xffff0000, v88
	v_mul_f32_e32 v87, v94, v87
	v_mul_f32_e32 v88, v95, v88
	v_med3_f32 v91, v87, s85, v240
	v_med3_f32 v88, v88, s85, v240
	v_mov_b32_e32 v87, 0
	v_cvt_pk_fp8_f32 v87, v91, v88
	v_pk_mul_f32 v[96:97], v[158:159], v[96:97] op_sel_hi:[0,1]
	v_lshlrev_b32_e32 v90, 16, v89
	v_and_b32_e32 v89, 0xffff0000, v89
	v_mul_f32_e32 v90, v96, v90
	v_mul_f32_e32 v88, v97, v89
	v_med3_f32 v89, v90, s85, v240
	v_med3_f32 v88, v88, s85, v240
	s_waitcnt lgkmcnt(1)
	v_pk_mul_f32 v[98:99], v[158:159], v[98:99] op_sel_hi:[0,1]
	v_cvt_pk_fp8_f32 v87, v89, v88 op_sel:[0,0,1]
	v_lshlrev_b32_e32 v88, 16, v82
	v_and_b32_e32 v82, 0xffff0000, v82
	v_mul_f32_e32 v88, v98, v88
	v_mul_f32_e32 v82, v99, v82
	v_med3_f32 v90, v88, s85, v240
	v_med3_f32 v82, v82, s85, v240
	v_mov_b32_e32 v88, 0
	v_cvt_pk_fp8_f32 v88, v90, v82
	v_pk_mul_f32 v[100:101], v[158:159], v[100:101] op_sel_hi:[0,1]
	v_lshlrev_b32_e32 v89, 16, v83
	v_and_b32_e32 v83, 0xffff0000, v83
	v_mul_f32_e32 v89, v100, v89
	v_mul_f32_e32 v82, v101, v83
	v_med3_f32 v83, v89, s85, v240
	v_med3_f32 v82, v82, s85, v240
	s_waitcnt lgkmcnt(0)
	v_pk_mul_f32 v[102:103], v[158:159], v[102:103] op_sel_hi:[0,1]
	v_cvt_pk_fp8_f32 v88, v83, v82 op_sel:[0,0,1]
	v_lshlrev_b32_e32 v82, 16, v84
	v_and_b32_e32 v83, 0xffff0000, v84
	v_mul_f32_e32 v82, v102, v82
	v_mul_f32_e32 v83, v103, v83
	v_med3_f32 v82, v82, s85, v240
	v_med3_f32 v83, v83, s85, v240
	v_mov_b32_e32 v89, 0
	v_cvt_pk_fp8_f32 v89, v82, v83
	v_pk_mul_f32 v[104:105], v[158:159], v[104:105] op_sel_hi:[0,1]
	v_lshlrev_b32_e32 v84, 16, v85
	v_and_b32_e32 v85, 0xffff0000, v85
	v_mul_f32_e32 v84, v104, v84
	v_mul_f32_e32 v82, v105, v85
	v_med3_f32 v83, v84, s85, v240
	v_med3_f32 v82, v82, s85, v240
	v_cvt_pk_fp8_f32 v89, v83, v82 op_sel:[0,0,1]
	global_store_dwordx4 v[164:165], v[86:89], off offset:-64
	ds_read_b128 v[82:85], v170 offset:2048
	ds_read_b128 v[86:89], v170 offset:2064
	ds_read_b128 v[90:93], v170 offset:2080
	ds_read_b128 v[94:97], v170 offset:2096
	v_lshlrev_b32_e32 v98, 16, v78
	s_waitcnt lgkmcnt(3)
	v_pk_mul_f32 v[82:83], v[158:159], v[82:83] op_sel_hi:[0,1]
	v_and_b32_e32 v78, 0xffff0000, v78
	v_pk_mul_f32 v[84:85], v[158:159], v[84:85] op_sel_hi:[0,1]
	v_mul_f32_e32 v82, v82, v98
	v_mul_f32_e32 v78, v83, v78
	v_lshlrev_b32_e32 v83, 16, v79
	v_mul_f32_e32 v83, v84, v83
	v_med3_f32 v82, v82, s85, v240
	v_med3_f32 v84, v78, s85, v240
	v_mov_b32_e32 v78, 0
	v_cvt_pk_fp8_f32 v78, v82, v84
	v_and_b32_e32 v79, 0xffff0000, v79
	v_mul_f32_e32 v79, v85, v79
	v_med3_f32 v82, v83, s85, v240
	v_med3_f32 v79, v79, s85, v240
	s_waitcnt lgkmcnt(2)
	v_pk_mul_f32 v[86:87], v[158:159], v[86:87] op_sel_hi:[0,1]
	v_cvt_pk_fp8_f32 v78, v82, v79 op_sel:[0,0,1]
	v_lshlrev_b32_e32 v79, 16, v80
	v_and_b32_e32 v80, 0xffff0000, v80
	v_mul_f32_e32 v79, v86, v79
	v_mul_f32_e32 v80, v87, v80
	v_med3_f32 v83, v79, s85, v240
	v_med3_f32 v80, v80, s85, v240
	v_mov_b32_e32 v79, 0
	v_cvt_pk_fp8_f32 v79, v83, v80
	v_pk_mul_f32 v[88:89], v[158:159], v[88:89] op_sel_hi:[0,1]
	v_lshlrev_b32_e32 v82, 16, v81
	v_and_b32_e32 v81, 0xffff0000, v81
	v_mul_f32_e32 v82, v88, v82
	v_mul_f32_e32 v80, v89, v81
	v_med3_f32 v81, v82, s85, v240
	v_med3_f32 v80, v80, s85, v240
	s_waitcnt lgkmcnt(1)
	v_pk_mul_f32 v[90:91], v[158:159], v[90:91] op_sel_hi:[0,1]
	v_cvt_pk_fp8_f32 v79, v81, v80 op_sel:[0,0,1]
	v_lshlrev_b32_e32 v80, 16, v74
	v_and_b32_e32 v74, 0xffff0000, v74
	v_mul_f32_e32 v80, v90, v80
	v_mul_f32_e32 v74, v91, v74
	v_med3_f32 v82, v80, s85, v240
	v_med3_f32 v74, v74, s85, v240
	v_mov_b32_e32 v80, 0
	v_cvt_pk_fp8_f32 v80, v82, v74
	v_pk_mul_f32 v[92:93], v[158:159], v[92:93] op_sel_hi:[0,1]
	v_lshlrev_b32_e32 v81, 16, v75
	v_and_b32_e32 v75, 0xffff0000, v75
	v_mul_f32_e32 v81, v92, v81
	v_mul_f32_e32 v74, v93, v75
	v_med3_f32 v75, v81, s85, v240
	v_med3_f32 v74, v74, s85, v240
	s_waitcnt lgkmcnt(0)
	v_pk_mul_f32 v[94:95], v[158:159], v[94:95] op_sel_hi:[0,1]
	v_cvt_pk_fp8_f32 v80, v75, v74 op_sel:[0,0,1]
	v_lshlrev_b32_e32 v74, 16, v76
	v_and_b32_e32 v75, 0xffff0000, v76
	v_mul_f32_e32 v74, v94, v74
	v_mul_f32_e32 v75, v95, v75
	v_med3_f32 v74, v74, s85, v240
	v_med3_f32 v75, v75, s85, v240
	v_mov_b32_e32 v81, 0
	v_cvt_pk_fp8_f32 v81, v74, v75
	v_pk_mul_f32 v[96:97], v[158:159], v[96:97] op_sel_hi:[0,1]
	v_lshlrev_b32_e32 v76, 16, v77
	v_and_b32_e32 v77, 0xffff0000, v77
	v_mul_f32_e32 v76, v96, v76
	v_mul_f32_e32 v74, v97, v77
	v_med3_f32 v75, v76, s85, v240
	v_med3_f32 v74, v74, s85, v240
	v_cvt_pk_fp8_f32 v81, v75, v74 op_sel:[0,0,1]
	global_store_dwordx4 v[164:165], v[78:81], off
	ds_read_b128 v[74:77], v170 offset:2304
	ds_read_b128 v[78:81], v170 offset:2320
	ds_read_b128 v[82:85], v170 offset:2336
	ds_read_b128 v[86:89], v170 offset:2352
	v_lshlrev_b32_e32 v90, 16, v70
	s_waitcnt lgkmcnt(3)
	v_pk_mul_f32 v[74:75], v[158:159], v[74:75] op_sel_hi:[0,1]
	v_and_b32_e32 v70, 0xffff0000, v70
	v_pk_mul_f32 v[76:77], v[158:159], v[76:77] op_sel_hi:[0,1]
	v_mul_f32_e32 v74, v74, v90
	v_mul_f32_e32 v70, v75, v70
	v_lshlrev_b32_e32 v75, 16, v71
	v_mul_f32_e32 v75, v76, v75
	v_med3_f32 v74, v74, s85, v240
	v_med3_f32 v76, v70, s85, v240
	v_mov_b32_e32 v70, 0
	v_cvt_pk_fp8_f32 v70, v74, v76
	v_and_b32_e32 v71, 0xffff0000, v71
	v_mul_f32_e32 v71, v77, v71
	v_med3_f32 v74, v75, s85, v240
	v_med3_f32 v71, v71, s85, v240
	s_waitcnt lgkmcnt(2)
	v_pk_mul_f32 v[78:79], v[158:159], v[78:79] op_sel_hi:[0,1]
	v_cvt_pk_fp8_f32 v70, v74, v71 op_sel:[0,0,1]
	v_lshlrev_b32_e32 v71, 16, v72
	v_and_b32_e32 v72, 0xffff0000, v72
	v_mul_f32_e32 v71, v78, v71
	v_mul_f32_e32 v72, v79, v72
	v_med3_f32 v75, v71, s85, v240
	v_med3_f32 v72, v72, s85, v240
	v_mov_b32_e32 v71, 0
	v_cvt_pk_fp8_f32 v71, v75, v72
	v_pk_mul_f32 v[80:81], v[158:159], v[80:81] op_sel_hi:[0,1]
	v_lshlrev_b32_e32 v74, 16, v73
	v_and_b32_e32 v73, 0xffff0000, v73
	v_mul_f32_e32 v74, v80, v74
	v_mul_f32_e32 v72, v81, v73
	v_med3_f32 v73, v74, s85, v240
	v_med3_f32 v72, v72, s85, v240
	s_waitcnt lgkmcnt(1)
	v_pk_mul_f32 v[82:83], v[158:159], v[82:83] op_sel_hi:[0,1]
	v_cvt_pk_fp8_f32 v71, v73, v72 op_sel:[0,0,1]
	v_lshlrev_b32_e32 v72, 16, v66
	v_and_b32_e32 v66, 0xffff0000, v66
	v_mul_f32_e32 v72, v82, v72
	v_mul_f32_e32 v66, v83, v66
	v_med3_f32 v74, v72, s85, v240
	v_med3_f32 v66, v66, s85, v240
	v_mov_b32_e32 v72, 0
	v_cvt_pk_fp8_f32 v72, v74, v66
	v_pk_mul_f32 v[84:85], v[158:159], v[84:85] op_sel_hi:[0,1]
	v_lshlrev_b32_e32 v73, 16, v67
	v_and_b32_e32 v67, 0xffff0000, v67
	v_mul_f32_e32 v73, v84, v73
	v_mul_f32_e32 v66, v85, v67
	v_med3_f32 v67, v73, s85, v240
	v_med3_f32 v66, v66, s85, v240
	s_waitcnt lgkmcnt(0)
	v_pk_mul_f32 v[86:87], v[158:159], v[86:87] op_sel_hi:[0,1]
	v_cvt_pk_fp8_f32 v72, v67, v66 op_sel:[0,0,1]
	v_lshlrev_b32_e32 v66, 16, v68
	v_and_b32_e32 v67, 0xffff0000, v68
	v_mul_f32_e32 v66, v86, v66
	v_mul_f32_e32 v67, v87, v67
	v_med3_f32 v66, v66, s85, v240
	v_med3_f32 v67, v67, s85, v240
	v_mov_b32_e32 v73, 0
	v_cvt_pk_fp8_f32 v73, v66, v67
	v_pk_mul_f32 v[88:89], v[158:159], v[88:89] op_sel_hi:[0,1]
	v_lshlrev_b32_e32 v68, 16, v69
	v_and_b32_e32 v69, 0xffff0000, v69
	v_mul_f32_e32 v68, v88, v68
	v_mul_f32_e32 v66, v89, v69
	v_med3_f32 v67, v68, s85, v240
	v_med3_f32 v66, v66, s85, v240
	v_cvt_pk_fp8_f32 v73, v67, v66 op_sel:[0,0,1]
	global_store_dwordx4 v[164:165], v[70:73], off offset:64
	ds_read_b128 v[66:69], v170 offset:2560
	ds_read_b128 v[70:73], v170 offset:2576
	ds_read_b128 v[74:77], v170 offset:2592
	ds_read_b128 v[78:81], v170 offset:2608
	v_lshlrev_b32_e32 v82, 16, v62
	s_waitcnt lgkmcnt(3)
	v_pk_mul_f32 v[66:67], v[158:159], v[66:67] op_sel_hi:[0,1]
	v_and_b32_e32 v62, 0xffff0000, v62
	v_pk_mul_f32 v[68:69], v[158:159], v[68:69] op_sel_hi:[0,1]
	v_mul_f32_e32 v66, v66, v82
	v_mul_f32_e32 v62, v67, v62
	v_lshlrev_b32_e32 v67, 16, v63
	v_mul_f32_e32 v67, v68, v67
	v_med3_f32 v66, v66, s85, v240
	v_med3_f32 v68, v62, s85, v240
	v_mov_b32_e32 v62, 0
	v_cvt_pk_fp8_f32 v62, v66, v68
	v_and_b32_e32 v63, 0xffff0000, v63
	v_mul_f32_e32 v63, v69, v63
	v_med3_f32 v66, v67, s85, v240
	v_med3_f32 v63, v63, s85, v240
	s_waitcnt lgkmcnt(2)
	v_pk_mul_f32 v[70:71], v[158:159], v[70:71] op_sel_hi:[0,1]
	v_cvt_pk_fp8_f32 v62, v66, v63 op_sel:[0,0,1]
	v_lshlrev_b32_e32 v63, 16, v64
	v_and_b32_e32 v64, 0xffff0000, v64
	v_mul_f32_e32 v63, v70, v63
	v_mul_f32_e32 v64, v71, v64
	v_med3_f32 v67, v63, s85, v240
	v_med3_f32 v64, v64, s85, v240
	v_mov_b32_e32 v63, 0
	v_cvt_pk_fp8_f32 v63, v67, v64
	v_pk_mul_f32 v[72:73], v[158:159], v[72:73] op_sel_hi:[0,1]
	v_lshlrev_b32_e32 v66, 16, v65
	v_and_b32_e32 v65, 0xffff0000, v65
	v_mul_f32_e32 v66, v72, v66
	v_mul_f32_e32 v64, v73, v65
	v_med3_f32 v65, v66, s85, v240
	v_med3_f32 v64, v64, s85, v240
	s_waitcnt lgkmcnt(1)
	v_pk_mul_f32 v[74:75], v[158:159], v[74:75] op_sel_hi:[0,1]
	v_cvt_pk_fp8_f32 v63, v65, v64 op_sel:[0,0,1]
	v_lshlrev_b32_e32 v64, 16, v58
	v_and_b32_e32 v58, 0xffff0000, v58
	v_mul_f32_e32 v64, v74, v64
	v_mul_f32_e32 v58, v75, v58
	v_med3_f32 v66, v64, s85, v240
	v_med3_f32 v58, v58, s85, v240
	v_mov_b32_e32 v64, 0
	v_cvt_pk_fp8_f32 v64, v66, v58
	v_pk_mul_f32 v[76:77], v[158:159], v[76:77] op_sel_hi:[0,1]
	v_lshlrev_b32_e32 v65, 16, v59
	v_and_b32_e32 v59, 0xffff0000, v59
	v_mul_f32_e32 v65, v76, v65
	v_mul_f32_e32 v58, v77, v59
	v_med3_f32 v59, v65, s85, v240
	v_med3_f32 v58, v58, s85, v240
	s_waitcnt lgkmcnt(0)
	v_pk_mul_f32 v[78:79], v[158:159], v[78:79] op_sel_hi:[0,1]
	v_cvt_pk_fp8_f32 v64, v59, v58 op_sel:[0,0,1]
	v_lshlrev_b32_e32 v58, 16, v60
	v_and_b32_e32 v59, 0xffff0000, v60
	v_mul_f32_e32 v58, v78, v58
	v_mul_f32_e32 v59, v79, v59
	v_med3_f32 v58, v58, s85, v240
	v_med3_f32 v59, v59, s85, v240
	v_mov_b32_e32 v65, 0
	v_cvt_pk_fp8_f32 v65, v58, v59
	v_pk_mul_f32 v[80:81], v[158:159], v[80:81] op_sel_hi:[0,1]
	v_lshlrev_b32_e32 v60, 16, v61
	v_and_b32_e32 v61, 0xffff0000, v61
	v_mul_f32_e32 v60, v80, v60
	v_mul_f32_e32 v58, v81, v61
	v_med3_f32 v59, v60, s85, v240
	v_med3_f32 v58, v58, s85, v240
	v_cvt_pk_fp8_f32 v65, v59, v58 op_sel:[0,0,1]
	global_store_dwordx4 v[164:165], v[62:65], off offset:128
	ds_read_b128 v[58:61], v170 offset:2816
	ds_read_b128 v[62:65], v170 offset:2832
	ds_read_b128 v[66:69], v170 offset:2848
	ds_read_b128 v[70:73], v170 offset:2864
	v_lshlrev_b32_e32 v74, 16, v38
	s_waitcnt lgkmcnt(3)
	v_pk_mul_f32 v[58:59], v[158:159], v[58:59] op_sel_hi:[0,1]
	v_and_b32_e32 v38, 0xffff0000, v38
	v_pk_mul_f32 v[60:61], v[158:159], v[60:61] op_sel_hi:[0,1]
	v_mul_f32_e32 v58, v58, v74
	v_mul_f32_e32 v38, v59, v38
	v_lshlrev_b32_e32 v59, 16, v39
	v_mul_f32_e32 v59, v60, v59
	v_med3_f32 v58, v58, s85, v240
	v_med3_f32 v60, v38, s85, v240
	v_mov_b32_e32 v38, 0
	v_cvt_pk_fp8_f32 v38, v58, v60
	v_and_b32_e32 v39, 0xffff0000, v39
	v_mul_f32_e32 v39, v61, v39
	v_med3_f32 v58, v59, s85, v240
	v_med3_f32 v39, v39, s85, v240
	s_waitcnt lgkmcnt(2)
	v_pk_mul_f32 v[62:63], v[158:159], v[62:63] op_sel_hi:[0,1]
	v_cvt_pk_fp8_f32 v38, v58, v39 op_sel:[0,0,1]
	v_lshlrev_b32_e32 v39, 16, v40
	v_and_b32_e32 v40, 0xffff0000, v40
	v_mul_f32_e32 v39, v62, v39
	v_mul_f32_e32 v40, v63, v40
	v_med3_f32 v59, v39, s85, v240
	v_med3_f32 v40, v40, s85, v240
	v_mov_b32_e32 v39, 0
	v_cvt_pk_fp8_f32 v39, v59, v40
	v_pk_mul_f32 v[64:65], v[158:159], v[64:65] op_sel_hi:[0,1]
	v_lshlrev_b32_e32 v58, 16, v41
	v_and_b32_e32 v41, 0xffff0000, v41
	v_mul_f32_e32 v58, v64, v58
	v_mul_f32_e32 v40, v65, v41
	v_med3_f32 v41, v58, s85, v240
	v_med3_f32 v40, v40, s85, v240
	s_waitcnt lgkmcnt(1)
	v_pk_mul_f32 v[66:67], v[158:159], v[66:67] op_sel_hi:[0,1]
	v_cvt_pk_fp8_f32 v39, v41, v40 op_sel:[0,0,1]
	v_lshlrev_b32_e32 v40, 16, v34
	v_and_b32_e32 v34, 0xffff0000, v34
	v_mul_f32_e32 v40, v66, v40
	v_mul_f32_e32 v34, v67, v34
	v_med3_f32 v58, v40, s85, v240
	v_med3_f32 v34, v34, s85, v240
	v_mov_b32_e32 v40, 0
	v_cvt_pk_fp8_f32 v40, v58, v34
	v_pk_mul_f32 v[68:69], v[158:159], v[68:69] op_sel_hi:[0,1]
	v_lshlrev_b32_e32 v41, 16, v35
	v_and_b32_e32 v35, 0xffff0000, v35
	v_mul_f32_e32 v41, v68, v41
	v_mul_f32_e32 v34, v69, v35
	v_med3_f32 v35, v41, s85, v240
	v_med3_f32 v34, v34, s85, v240
	s_waitcnt lgkmcnt(0)
	v_pk_mul_f32 v[70:71], v[158:159], v[70:71] op_sel_hi:[0,1]
	v_cvt_pk_fp8_f32 v40, v35, v34 op_sel:[0,0,1]
	v_lshlrev_b32_e32 v34, 16, v36
	v_and_b32_e32 v35, 0xffff0000, v36
	v_mul_f32_e32 v34, v70, v34
	v_mul_f32_e32 v35, v71, v35
	v_med3_f32 v34, v34, s85, v240
	v_med3_f32 v35, v35, s85, v240
	v_mov_b32_e32 v41, 0
	v_cvt_pk_fp8_f32 v41, v34, v35
	v_pk_mul_f32 v[72:73], v[158:159], v[72:73] op_sel_hi:[0,1]
	v_lshlrev_b32_e32 v36, 16, v37
	v_and_b32_e32 v37, 0xffff0000, v37
	v_mul_f32_e32 v36, v72, v36
	v_mul_f32_e32 v34, v73, v37
	v_med3_f32 v35, v36, s85, v240
	v_med3_f32 v34, v34, s85, v240
	v_cvt_pk_fp8_f32 v41, v35, v34 op_sel:[0,0,1]
	global_store_dwordx4 v[164:165], v[38:41], off offset:192
	ds_read_b128 v[34:37], v170 offset:3072
	ds_read_b128 v[38:41], v170 offset:3088
	ds_read_b128 v[58:61], v170 offset:3104
	ds_read_b128 v[62:65], v170 offset:3120
	v_lshlrev_b32_e32 v66, 16, v30
	s_waitcnt lgkmcnt(3)
	v_pk_mul_f32 v[34:35], v[158:159], v[34:35] op_sel_hi:[0,1]
	v_and_b32_e32 v30, 0xffff0000, v30
	v_pk_mul_f32 v[36:37], v[158:159], v[36:37] op_sel_hi:[0,1]
	v_mul_f32_e32 v34, v34, v66
	v_mul_f32_e32 v30, v35, v30
	v_lshlrev_b32_e32 v35, 16, v31
	v_mul_f32_e32 v35, v36, v35
	v_med3_f32 v34, v34, s85, v240
	v_med3_f32 v36, v30, s85, v240
	v_mov_b32_e32 v30, 0
	v_cvt_pk_fp8_f32 v30, v34, v36
	v_and_b32_e32 v31, 0xffff0000, v31
	v_mul_f32_e32 v31, v37, v31
	v_med3_f32 v34, v35, s85, v240
	v_med3_f32 v31, v31, s85, v240
	s_waitcnt lgkmcnt(2)
	v_pk_mul_f32 v[38:39], v[158:159], v[38:39] op_sel_hi:[0,1]
	v_cvt_pk_fp8_f32 v30, v34, v31 op_sel:[0,0,1]
	v_lshlrev_b32_e32 v31, 16, v32
	v_and_b32_e32 v32, 0xffff0000, v32
	v_mul_f32_e32 v31, v38, v31
	v_mul_f32_e32 v32, v39, v32
	v_med3_f32 v35, v31, s85, v240
	v_med3_f32 v32, v32, s85, v240
	v_mov_b32_e32 v31, 0
	v_cvt_pk_fp8_f32 v31, v35, v32
	v_pk_mul_f32 v[40:41], v[158:159], v[40:41] op_sel_hi:[0,1]
	v_lshlrev_b32_e32 v34, 16, v33
	v_and_b32_e32 v33, 0xffff0000, v33
	v_mul_f32_e32 v34, v40, v34
	v_mul_f32_e32 v32, v41, v33
	v_med3_f32 v33, v34, s85, v240
	v_med3_f32 v32, v32, s85, v240
	s_waitcnt lgkmcnt(1)
	v_pk_mul_f32 v[58:59], v[158:159], v[58:59] op_sel_hi:[0,1]
	v_cvt_pk_fp8_f32 v31, v33, v32 op_sel:[0,0,1]
	v_lshlrev_b32_e32 v32, 16, v26
	v_and_b32_e32 v26, 0xffff0000, v26
	v_mul_f32_e32 v32, v58, v32
	v_mul_f32_e32 v26, v59, v26
	v_med3_f32 v34, v32, s85, v240
	v_med3_f32 v26, v26, s85, v240
	v_mov_b32_e32 v32, 0
	v_cvt_pk_fp8_f32 v32, v34, v26
	v_pk_mul_f32 v[60:61], v[158:159], v[60:61] op_sel_hi:[0,1]
	v_lshlrev_b32_e32 v33, 16, v27
	v_and_b32_e32 v27, 0xffff0000, v27
	v_mul_f32_e32 v33, v60, v33
	v_mul_f32_e32 v26, v61, v27
	v_med3_f32 v27, v33, s85, v240
	v_med3_f32 v26, v26, s85, v240
	s_waitcnt lgkmcnt(0)
	v_pk_mul_f32 v[62:63], v[158:159], v[62:63] op_sel_hi:[0,1]
	v_cvt_pk_fp8_f32 v32, v27, v26 op_sel:[0,0,1]
	v_lshlrev_b32_e32 v26, 16, v28
	v_and_b32_e32 v27, 0xffff0000, v28
	v_mul_f32_e32 v26, v62, v26
	v_mul_f32_e32 v27, v63, v27
	v_med3_f32 v26, v26, s85, v240
	v_med3_f32 v27, v27, s85, v240
	v_mov_b32_e32 v33, 0
	v_cvt_pk_fp8_f32 v33, v26, v27
	v_pk_mul_f32 v[64:65], v[158:159], v[64:65] op_sel_hi:[0,1]
	v_lshlrev_b32_e32 v28, 16, v29
	v_and_b32_e32 v29, 0xffff0000, v29
	v_mul_f32_e32 v28, v64, v28
	v_mul_f32_e32 v26, v65, v29
	v_med3_f32 v27, v28, s85, v240
	v_med3_f32 v26, v26, s85, v240
	v_cvt_pk_fp8_f32 v33, v27, v26 op_sel:[0,0,1]
	global_store_dwordx4 v[164:165], v[30:33], off offset:256
	ds_read_b128 v[26:29], v170 offset:3328
	ds_read_b128 v[30:33], v170 offset:3344
	ds_read_b128 v[34:37], v170 offset:3360
	ds_read_b128 v[38:41], v170 offset:3376
	v_lshlrev_b32_e32 v58, 16, v22
	s_waitcnt lgkmcnt(3)
	v_pk_mul_f32 v[26:27], v[158:159], v[26:27] op_sel_hi:[0,1]
	v_and_b32_e32 v22, 0xffff0000, v22
	v_pk_mul_f32 v[28:29], v[158:159], v[28:29] op_sel_hi:[0,1]
	v_mul_f32_e32 v26, v26, v58
	v_mul_f32_e32 v22, v27, v22
	v_lshlrev_b32_e32 v27, 16, v23
	v_mul_f32_e32 v27, v28, v27
	v_med3_f32 v26, v26, s85, v240
	v_med3_f32 v28, v22, s85, v240
	v_mov_b32_e32 v22, 0
	v_cvt_pk_fp8_f32 v22, v26, v28
	v_and_b32_e32 v23, 0xffff0000, v23
	v_mul_f32_e32 v23, v29, v23
	v_med3_f32 v26, v27, s85, v240
	v_med3_f32 v23, v23, s85, v240
	s_waitcnt lgkmcnt(2)
	v_pk_mul_f32 v[30:31], v[158:159], v[30:31] op_sel_hi:[0,1]
	v_cvt_pk_fp8_f32 v22, v26, v23 op_sel:[0,0,1]
	v_lshlrev_b32_e32 v23, 16, v24
	v_and_b32_e32 v24, 0xffff0000, v24
	v_mul_f32_e32 v23, v30, v23
	v_mul_f32_e32 v24, v31, v24
	v_med3_f32 v27, v23, s85, v240
	v_med3_f32 v24, v24, s85, v240
	v_mov_b32_e32 v23, 0
	v_cvt_pk_fp8_f32 v23, v27, v24
	v_pk_mul_f32 v[32:33], v[158:159], v[32:33] op_sel_hi:[0,1]
	v_lshlrev_b32_e32 v26, 16, v25
	v_and_b32_e32 v25, 0xffff0000, v25
	v_mul_f32_e32 v26, v32, v26
	v_mul_f32_e32 v24, v33, v25
	v_med3_f32 v25, v26, s85, v240
	v_med3_f32 v24, v24, s85, v240
	s_waitcnt lgkmcnt(1)
	v_pk_mul_f32 v[34:35], v[158:159], v[34:35] op_sel_hi:[0,1]
	v_cvt_pk_fp8_f32 v23, v25, v24 op_sel:[0,0,1]
	v_lshlrev_b32_e32 v24, 16, v18
	v_and_b32_e32 v18, 0xffff0000, v18
	v_mul_f32_e32 v24, v34, v24
	v_mul_f32_e32 v18, v35, v18
	v_med3_f32 v26, v24, s85, v240
	v_med3_f32 v18, v18, s85, v240
	v_mov_b32_e32 v24, 0
	v_cvt_pk_fp8_f32 v24, v26, v18
	v_pk_mul_f32 v[36:37], v[158:159], v[36:37] op_sel_hi:[0,1]
	v_lshlrev_b32_e32 v25, 16, v19
	v_and_b32_e32 v19, 0xffff0000, v19
	v_mul_f32_e32 v25, v36, v25
	v_mul_f32_e32 v18, v37, v19
	v_med3_f32 v19, v25, s85, v240
	v_med3_f32 v18, v18, s85, v240
	s_waitcnt lgkmcnt(0)
	v_pk_mul_f32 v[38:39], v[158:159], v[38:39] op_sel_hi:[0,1]
	v_cvt_pk_fp8_f32 v24, v19, v18 op_sel:[0,0,1]
	v_lshlrev_b32_e32 v18, 16, v20
	v_and_b32_e32 v19, 0xffff0000, v20
	v_mul_f32_e32 v18, v38, v18
	v_mul_f32_e32 v19, v39, v19
	v_med3_f32 v18, v18, s85, v240
	v_med3_f32 v19, v19, s85, v240
	v_mov_b32_e32 v25, 0
	v_cvt_pk_fp8_f32 v25, v18, v19
	v_pk_mul_f32 v[40:41], v[158:159], v[40:41] op_sel_hi:[0,1]
	v_lshlrev_b32_e32 v20, 16, v21
	v_and_b32_e32 v21, 0xffff0000, v21
	v_mul_f32_e32 v20, v40, v20
	v_mul_f32_e32 v18, v41, v21
	v_med3_f32 v19, v20, s85, v240
	v_med3_f32 v18, v18, s85, v240
	v_cvt_pk_fp8_f32 v25, v19, v18 op_sel:[0,0,1]
	global_store_dwordx4 v[164:165], v[22:25], off offset:320
	ds_read_b128 v[18:21], v170 offset:3584
	ds_read_b128 v[22:25], v170 offset:3600
	ds_read_b128 v[26:29], v170 offset:3616
	ds_read_b128 v[30:33], v170 offset:3632
	v_lshlrev_b32_e32 v34, 16, v14
	s_waitcnt lgkmcnt(3)
	v_pk_mul_f32 v[18:19], v[158:159], v[18:19] op_sel_hi:[0,1]
	v_and_b32_e32 v14, 0xffff0000, v14
	v_pk_mul_f32 v[20:21], v[158:159], v[20:21] op_sel_hi:[0,1]
	v_mul_f32_e32 v18, v18, v34
	v_mul_f32_e32 v14, v19, v14
	v_lshlrev_b32_e32 v19, 16, v15
	v_mul_f32_e32 v19, v20, v19
	v_med3_f32 v18, v18, s85, v240
	v_med3_f32 v20, v14, s85, v240
	v_mov_b32_e32 v14, 0
	v_cvt_pk_fp8_f32 v14, v18, v20
	v_and_b32_e32 v15, 0xffff0000, v15
	v_mul_f32_e32 v15, v21, v15
	v_med3_f32 v18, v19, s85, v240
	v_med3_f32 v15, v15, s85, v240
	s_waitcnt lgkmcnt(2)
	v_pk_mul_f32 v[22:23], v[158:159], v[22:23] op_sel_hi:[0,1]
	v_cvt_pk_fp8_f32 v14, v18, v15 op_sel:[0,0,1]
	v_lshlrev_b32_e32 v15, 16, v16
	v_and_b32_e32 v16, 0xffff0000, v16
	v_mul_f32_e32 v15, v22, v15
	v_mul_f32_e32 v16, v23, v16
	v_med3_f32 v19, v15, s85, v240
	v_med3_f32 v16, v16, s85, v240
	v_mov_b32_e32 v15, 0
	v_cvt_pk_fp8_f32 v15, v19, v16
	v_pk_mul_f32 v[24:25], v[158:159], v[24:25] op_sel_hi:[0,1]
	v_lshlrev_b32_e32 v18, 16, v17
	v_and_b32_e32 v17, 0xffff0000, v17
	v_mul_f32_e32 v18, v24, v18
	v_mul_f32_e32 v16, v25, v17
	v_med3_f32 v17, v18, s85, v240
	v_med3_f32 v16, v16, s85, v240
	s_waitcnt lgkmcnt(1)
	v_pk_mul_f32 v[26:27], v[158:159], v[26:27] op_sel_hi:[0,1]
	v_cvt_pk_fp8_f32 v15, v17, v16 op_sel:[0,0,1]
	v_lshlrev_b32_e32 v16, 16, v10
	v_and_b32_e32 v10, 0xffff0000, v10
	v_mul_f32_e32 v16, v26, v16
	v_mul_f32_e32 v10, v27, v10
	v_med3_f32 v18, v16, s85, v240
	v_med3_f32 v10, v10, s85, v240
	v_mov_b32_e32 v16, 0
	v_cvt_pk_fp8_f32 v16, v18, v10
	v_pk_mul_f32 v[28:29], v[158:159], v[28:29] op_sel_hi:[0,1]
	v_lshlrev_b32_e32 v17, 16, v11
	v_and_b32_e32 v11, 0xffff0000, v11
	v_mul_f32_e32 v17, v28, v17
	v_mul_f32_e32 v10, v29, v11
	v_med3_f32 v11, v17, s85, v240
	v_med3_f32 v10, v10, s85, v240
	s_waitcnt lgkmcnt(0)
	v_pk_mul_f32 v[30:31], v[158:159], v[30:31] op_sel_hi:[0,1]
	v_cvt_pk_fp8_f32 v16, v11, v10 op_sel:[0,0,1]
	v_lshlrev_b32_e32 v10, 16, v12
	v_and_b32_e32 v11, 0xffff0000, v12
	v_mul_f32_e32 v10, v30, v10
	v_mul_f32_e32 v11, v31, v11
	v_med3_f32 v10, v10, s85, v240
	v_med3_f32 v11, v11, s85, v240
	v_mov_b32_e32 v17, 0
	v_cvt_pk_fp8_f32 v17, v10, v11
	v_pk_mul_f32 v[32:33], v[158:159], v[32:33] op_sel_hi:[0,1]
	v_lshlrev_b32_e32 v12, 16, v13
	v_and_b32_e32 v13, 0xffff0000, v13
	v_mul_f32_e32 v12, v32, v12
	v_mul_f32_e32 v10, v33, v13
	v_med3_f32 v11, v12, s85, v240
	v_med3_f32 v10, v10, s85, v240
	v_cvt_pk_fp8_f32 v17, v11, v10 op_sel:[0,0,1]
	global_store_dwordx4 v[164:165], v[14:17], off offset:384
	v_mov_b64_e32 v[12:13], v[4:5]
	v_mov_b64_e32 v[10:11], v[2:3]
	ds_read_b128 v[14:17], v170 offset:3840
	ds_read_b128 v[18:21], v170 offset:3856
	ds_read_b128 v[22:25], v170 offset:3872
	ds_read_b128 v[26:29], v170 offset:3888
	v_lshlrev_b32_e32 v30, 16, v6
	s_waitcnt lgkmcnt(3)
	v_pk_mul_f32 v[14:15], v[158:159], v[14:15] op_sel_hi:[0,1]
	v_and_b32_e32 v6, 0xffff0000, v6
	v_pk_mul_f32 v[16:17], v[158:159], v[16:17] op_sel_hi:[0,1]
	v_mul_f32_e32 v14, v14, v30
	v_mul_f32_e32 v6, v15, v6
	v_lshlrev_b32_e32 v15, 16, v7
	v_mul_f32_e32 v15, v16, v15
	v_med3_f32 v14, v14, s85, v240
	v_med3_f32 v16, v6, s85, v240
	v_mov_b32_e32 v6, 0
	v_cvt_pk_fp8_f32 v6, v14, v16
	v_and_b32_e32 v7, 0xffff0000, v7
	v_mul_f32_e32 v7, v17, v7
	v_med3_f32 v14, v15, s85, v240
	v_med3_f32 v7, v7, s85, v240
	s_waitcnt lgkmcnt(2)
	v_pk_mul_f32 v[18:19], v[158:159], v[18:19] op_sel_hi:[0,1]
	v_cvt_pk_fp8_f32 v6, v14, v7 op_sel:[0,0,1]
	v_lshlrev_b32_e32 v7, 16, v8
	v_and_b32_e32 v8, 0xffff0000, v8
	v_mul_f32_e32 v7, v18, v7
	v_mul_f32_e32 v8, v19, v8
	v_med3_f32 v15, v7, s85, v240
	v_med3_f32 v8, v8, s85, v240
	v_mov_b32_e32 v7, 0
	v_cvt_pk_fp8_f32 v7, v15, v8
	v_pk_mul_f32 v[20:21], v[158:159], v[20:21] op_sel_hi:[0,1]
	v_lshlrev_b32_e32 v14, 16, v9
	v_and_b32_e32 v9, 0xffff0000, v9
	v_mul_f32_e32 v14, v20, v14
	v_mul_f32_e32 v8, v21, v9
	v_med3_f32 v9, v14, s85, v240
	v_med3_f32 v8, v8, s85, v240
	s_waitcnt lgkmcnt(1)
	v_pk_mul_f32 v[22:23], v[158:159], v[22:23] op_sel_hi:[0,1]
	v_cvt_pk_fp8_f32 v7, v9, v8 op_sel:[0,0,1]
	v_lshlrev_b32_e32 v8, 16, v10
	v_and_b32_e32 v9, 0xffff0000, v10
	v_mul_f32_e32 v8, v22, v8
	v_mul_f32_e32 v9, v23, v9
	v_med3_f32 v14, v8, s85, v240
	v_med3_f32 v9, v9, s85, v240
	v_mov_b32_e32 v8, 0
	v_cvt_pk_fp8_f32 v8, v14, v9
	v_pk_mul_f32 v[24:25], v[158:159], v[24:25] op_sel_hi:[0,1]
	v_lshlrev_b32_e32 v10, 16, v11
	v_and_b32_e32 v11, 0xffff0000, v11
	v_mul_f32_e32 v10, v24, v10
	v_mul_f32_e32 v9, v25, v11
	v_med3_f32 v10, v10, s85, v240
	v_med3_f32 v9, v9, s85, v240
	s_waitcnt lgkmcnt(0)
	v_pk_mul_f32 v[26:27], v[158:159], v[26:27] op_sel_hi:[0,1]
	v_cvt_pk_fp8_f32 v8, v10, v9 op_sel:[0,0,1]
	v_lshlrev_b32_e32 v9, 16, v12
	v_and_b32_e32 v10, 0xffff0000, v12
	v_mul_f32_e32 v9, v26, v9
	v_mul_f32_e32 v10, v27, v10
	v_lshlrev_b32_e32 v11, 16, v13
	v_and_b32_e32 v12, 0xffff0000, v13
	v_med3_f32 v13, v9, s85, v240
	v_med3_f32 v10, v10, s85, v240
	v_mov_b32_e32 v9, 0
	v_cvt_pk_fp8_f32 v9, v13, v10
	v_pk_mul_f32 v[28:29], v[158:159], v[28:29] op_sel_hi:[0,1]
	v_mul_f32_e32 v11, v28, v11
	v_mul_f32_e32 v10, v29, v12
	v_med3_f32 v11, v11, s85, v240
	v_med3_f32 v10, v10, s85, v240
	v_cvt_pk_fp8_f32 v9, v11, v10 op_sel:[0,0,1]
	global_store_dwordx4 v[164:165], v[6:9], off offset:448
	s_nop 1
	v_mfma_f32_16x16x32_bf16 v[6:9], v[2:5], v[46:49], v[42:45]
	v_mfma_f32_16x16x32_bf16 v[2:5], v[2:5], v[50:53], v[54:57]
	ds_bpermute_b32 v14, v228, v158
	s_nop 6
	v_pk_add_f32 v[2:3], v[6:7], v[2:3]
	ds_bpermute_b32 v6, v230, v158
	v_pk_add_f32 v[12:13], v[118:119], v[130:131]
	v_pk_add_f32 v[10:11], v[120:121], v[132:133]
	s_waitcnt lgkmcnt(1)
	v_fma_f32 v7, v12, v14, v1
	v_fma_f32 v2, v2, v14, v168
	ds_write2_b32 v229, v7, v2 offset1:16
	ds_bpermute_b32 v2, v232, v158
	s_waitcnt lgkmcnt(2)
	v_fma_f32 v7, v13, v6, v1
	v_fma_f32 v3, v3, v6, v168
	ds_bpermute_b32 v6, v234, v158
	v_pk_add_f32 v[4:5], v[8:9], v[4:5]
	ds_write2_b32 v231, v7, v3 offset1:16
	s_waitcnt lgkmcnt(2)
	v_fma_f32 v3, v10, v2, v1
	v_fma_f32 v2, v4, v2, v168
	ds_write2_b32 v233, v3, v2 offset1:16
	s_waitcnt lgkmcnt(2)
	v_fma_f32 v2, v11, v6, v1
	v_fma_f32 v3, v5, v6, v168
	ds_write2_b32 v235, v2, v3 offset1:16
	ds_read2_b32 v[2:3], v238 offset1:1
	ds_read2_b32 v[32:33], v238 offset0:2 offset1:3
	ds_read2_b32 v[30:31], v238 offset0:4 offset1:5
	ds_read2_b32 v[28:29], v238 offset0:6 offset1:7
	ds_read2_b32 v[26:27], v238 offset0:8 offset1:9
	ds_read2_b32 v[24:25], v238 offset0:10 offset1:11
	ds_read2_b32 v[22:23], v238 offset0:12 offset1:13
	ds_read2_b32 v[20:21], v238 offset0:14 offset1:15
	ds_read2_b32 v[18:19], v238 offset0:16 offset1:17
	ds_read2_b32 v[16:17], v238 offset0:18 offset1:19
	ds_read2_b32 v[14:15], v238 offset0:20 offset1:21
	ds_read2_b32 v[12:13], v238 offset0:22 offset1:23
	ds_read2_b32 v[10:11], v238 offset0:24 offset1:25
	ds_read2_b32 v[8:9], v238 offset0:26 offset1:27
	ds_read2_b32 v[6:7], v238 offset0:28 offset1:29
	ds_read2_b32 v[4:5], v238 offset0:30 offset1:31
	s_and_saveexec_b64 s[94:95], s[0:1]
	s_cbranch_execz .LBB0_931
	s_waitcnt lgkmcnt(14)
	v_cmp_lg_f32_e32 vcc, s89, v2
	v_cmp_lg_f32_e64 s[46:47], s89, v3
	v_ashrrev_i32_e32 v163, 31, v162
	v_cndmask_b32_e32 v34, v241, v2, vcc
	v_cmp_gt_f32_e64 s[10:11], v3, v34
	v_cmp_ngt_f32_e64 s[44:45], v3, v34
	s_nop 0
	v_cndmask_b32_e64 v35, v34, v3, s[10:11]
	v_cndmask_b32_e64 v3, v241, v3, s[46:47]
	v_cndmask_b32_e64 v94, v3, v34, s[10:11]
	v_cmp_gt_f32_e64 s[40:41], v32, v94
	v_cmp_gt_f32_e64 s[48:49], v32, v35
	v_cndmask_b32_e64 v65, 0, 1, s[10:11]
	v_cndmask_b32_e64 v3, v94, v32, s[40:41]
	v_cndmask_b32_e64 v95, v3, v35, s[48:49]
	v_cndmask_b32_e64 v36, v35, v32, s[48:49]
	v_cmp_gt_f32_e64 s[38:39], v33, v95
	v_cmp_gt_f32_e64 s[50:51], v33, v36
	s_and_b64 s[46:47], s[46:47], s[44:45]
	v_cndmask_b32_e64 v3, v95, v33, s[38:39]
	v_cndmask_b32_e64 v96, v3, v36, s[50:51]
	v_cndmask_b32_e64 v37, v36, v33, s[50:51]
	s_waitcnt lgkmcnt(13)
	v_cmp_gt_f32_e64 s[30:31], v30, v96
	v_cmp_gt_f32_e64 s[52:53], v30, v37
	v_cndmask_b32_e64 v97, 0, 1, s[46:47]
	v_cndmask_b32_e64 v3, v96, v30, s[30:31]
	v_cndmask_b32_e64 v38, v37, v30, s[52:53]
	v_cndmask_b32_e64 v37, v3, v37, s[52:53]
	v_cmp_gt_f32_e64 s[28:29], v31, v37
	v_cmp_gt_f32_e64 s[54:55], v31, v38
	v_cndmask_b32_e64 v66, v65, 2, s[48:49]
	v_cndmask_b32_e64 v3, v37, v31, s[28:29]
	v_cndmask_b32_e64 v39, v38, v31, s[54:55]
	v_cndmask_b32_e64 v38, v3, v38, s[54:55]
	s_waitcnt lgkmcnt(12)
	v_cmp_gt_f32_e64 s[24:25], v28, v38
	v_cmp_gt_f32_e64 s[56:57], v28, v39
	v_cndmask_b32_e64 v67, v66, 3, s[50:51]
	v_cndmask_b32_e64 v3, v38, v28, s[24:25]
	v_cndmask_b32_e64 v40, v39, v28, s[56:57]
	v_cndmask_b32_e64 v39, v3, v39, s[56:57]
	v_cmp_gt_f32_e64 s[22:23], v29, v39
	v_cmp_gt_f32_e64 s[60:61], v29, v40
	v_cndmask_b32_e64 v68, v67, 4, s[52:53]
	v_cndmask_b32_e64 v3, v39, v29, s[22:23]
	v_cndmask_b32_e64 v41, v40, v29, s[60:61]
	v_cndmask_b32_e64 v40, v3, v40, s[60:61]
	s_waitcnt lgkmcnt(11)
	v_cmp_gt_f32_e64 s[18:19], v26, v40
	v_cmp_gt_f32_e64 s[62:63], v26, v41
	v_cndmask_b32_e64 v69, v68, 5, s[54:55]
	v_cndmask_b32_e64 v3, v40, v26, s[18:19]
	v_cndmask_b32_e64 v42, v41, v26, s[62:63]
	v_cndmask_b32_e64 v41, v3, v41, s[62:63]
	v_cmp_gt_f32_e64 s[16:17], v27, v41
	v_cmp_gt_f32_e64 s[64:65], v27, v42
	v_cndmask_b32_e64 v70, v69, 6, s[56:57]
	v_cndmask_b32_e64 v3, v41, v27, s[16:17]
	v_cndmask_b32_e64 v43, v42, v27, s[64:65]
	v_cndmask_b32_e64 v42, v3, v42, s[64:65]
	s_waitcnt lgkmcnt(10)
	v_cmp_gt_f32_e64 s[12:13], v24, v42
	v_cmp_gt_f32_e64 s[66:67], v24, v43
	v_cndmask_b32_e64 v71, v70, 7, s[60:61]
	v_cndmask_b32_e64 v3, v42, v24, s[12:13]
	v_cndmask_b32_e64 v44, v43, v24, s[66:67]
	v_cndmask_b32_e64 v43, v3, v43, s[66:67]
	v_cmp_gt_f32_e64 s[10:11], v25, v43
	v_cmp_gt_f32_e64 s[68:69], v25, v44
	v_cndmask_b32_e64 v72, v71, 8, s[62:63]
	v_cndmask_b32_e64 v3, v43, v25, s[10:11]
	v_cndmask_b32_e64 v45, v44, v25, s[68:69]
	v_cndmask_b32_e64 v44, v3, v44, s[68:69]
	s_waitcnt lgkmcnt(9)
	v_cmp_gt_f32_e64 s[44:45], v22, v44
	v_cmp_gt_f32_e64 s[70:71], v22, v45
	v_cndmask_b32_e64 v73, v72, 9, s[64:65]
	v_cndmask_b32_e64 v3, v44, v22, s[44:45]
	v_cndmask_b32_e64 v46, v45, v22, s[70:71]
	v_cndmask_b32_e64 v45, v3, v45, s[70:71]
	v_cmp_gt_f32_e64 s[46:47], v23, v45
	v_cmp_gt_f32_e64 s[72:73], v23, v46
	v_cndmask_b32_e64 v74, v73, 10, s[66:67]
	v_cndmask_b32_e64 v3, v45, v23, s[46:47]
	v_cndmask_b32_e64 v47, v46, v23, s[72:73]
	v_cndmask_b32_e64 v46, v3, v46, s[72:73]
	v_cndmask_b32_e64 v3, v97, 2, s[40:41]
	v_cndmask_b32_e64 v65, v3, v65, s[48:49]
	s_waitcnt lgkmcnt(8)
	v_cmp_gt_f32_e64 s[48:49], v20, v46
	v_cmp_gt_f32_e64 s[74:75], v20, v47
	v_cndmask_b32_e64 v75, v74, 11, s[68:69]
	v_cndmask_b32_e64 v3, v46, v20, s[48:49]
	v_cndmask_b32_e64 v48, v47, v20, s[74:75]
	v_cndmask_b32_e64 v47, v3, v47, s[74:75]
	v_cndmask_b32_e64 v3, v65, 3, s[38:39]
	v_cndmask_b32_e64 v66, v3, v66, s[50:51]
	v_cmp_gt_f32_e64 s[50:51], v21, v47
	v_cmp_gt_f32_e64 s[76:77], v21, v48
	v_cndmask_b32_e64 v76, v75, 12, s[70:71]
	v_cndmask_b32_e64 v3, v47, v21, s[50:51]
	v_cndmask_b32_e64 v49, v48, v21, s[76:77]
	v_cndmask_b32_e64 v48, v3, v48, s[76:77]
	v_cndmask_b32_e64 v3, v66, 4, s[30:31]
	v_cndmask_b32_e64 v67, v3, v67, s[52:53]
	s_waitcnt lgkmcnt(7)
	v_cmp_gt_f32_e64 s[52:53], v18, v48
	v_cmp_gt_f32_e64 s[78:79], v18, v49
	v_cndmask_b32_e64 v77, v76, 13, s[72:73]
	v_cndmask_b32_e64 v3, v48, v18, s[52:53]
	v_cndmask_b32_e64 v50, v49, v18, s[78:79]
	v_cndmask_b32_e64 v49, v3, v49, s[78:79]
	v_cndmask_b32_e64 v3, v67, 5, s[28:29]
	v_cndmask_b32_e64 v68, v3, v68, s[54:55]
	v_cmp_gt_f32_e64 s[54:55], v19, v49
	v_cmp_gt_f32_e64 s[82:83], v19, v50
	v_cndmask_b32_e64 v78, v77, 14, s[74:75]
	v_cndmask_b32_e64 v3, v49, v19, s[54:55]
	v_cndmask_b32_e64 v51, v50, v19, s[82:83]
	v_cndmask_b32_e64 v50, v3, v50, s[82:83]
	v_cndmask_b32_e64 v3, v68, 6, s[24:25]
	v_cndmask_b32_e64 v69, v3, v69, s[56:57]
	s_waitcnt lgkmcnt(6)
	v_cmp_gt_f32_e64 s[56:57], v16, v50
	v_cmp_gt_f32_e64 s[80:81], v16, v51
	v_cndmask_b32_e64 v79, v78, 15, s[76:77]
	v_cndmask_b32_e64 v3, v50, v16, s[56:57]
	v_cndmask_b32_e64 v52, v51, v16, s[80:81]
	v_cndmask_b32_e64 v51, v3, v51, s[80:81]
	v_cndmask_b32_e64 v3, v69, 7, s[22:23]
	v_cndmask_b32_e64 v70, v3, v70, s[60:61]
	v_cmp_gt_f32_e64 s[60:61], v17, v51
	v_cmp_gt_f32_e32 vcc, v17, v52
	v_cndmask_b32_e64 v80, v79, 16, s[78:79]
	v_cndmask_b32_e64 v3, v51, v17, s[60:61]
	v_cndmask_b32_e32 v53, v52, v17, vcc
	v_cndmask_b32_e32 v52, v3, v52, vcc
	v_cndmask_b32_e64 v3, v70, 8, s[18:19]
	v_cndmask_b32_e64 v71, v3, v71, s[62:63]
	s_waitcnt lgkmcnt(5)
	v_cmp_gt_f32_e64 s[62:63], v14, v52
	v_cmp_gt_f32_e64 s[2:3], v14, v53
	v_cndmask_b32_e64 v81, v80, 17, s[82:83]
	v_cndmask_b32_e64 v3, v52, v14, s[62:63]
	v_cndmask_b32_e64 v54, v53, v14, s[2:3]
	v_cndmask_b32_e64 v53, v3, v53, s[2:3]
	v_cndmask_b32_e64 v3, v71, 9, s[16:17]
	v_cndmask_b32_e64 v72, v3, v72, s[64:65]
	v_cmp_gt_f32_e64 s[64:65], v15, v53
	v_cmp_gt_f32_e64 s[4:5], v15, v54
	v_cndmask_b32_e64 v82, v81, 18, s[80:81]
	v_cndmask_b32_e64 v3, v53, v15, s[64:65]
	v_cndmask_b32_e64 v55, v54, v15, s[4:5]
	v_cndmask_b32_e64 v54, v3, v54, s[4:5]
	v_cndmask_b32_e64 v3, v72, 10, s[12:13]
	v_cndmask_b32_e64 v73, v3, v73, s[66:67]
	s_waitcnt lgkmcnt(4)
	v_cmp_gt_f32_e64 s[66:67], v12, v54
	v_cmp_gt_f32_e64 s[6:7], v12, v55
	v_cndmask_b32_e64 v83, v82, 19, vcc
	v_cndmask_b32_e64 v3, v54, v12, s[66:67]
	v_cndmask_b32_e64 v56, v55, v12, s[6:7]
	v_cndmask_b32_e64 v55, v3, v55, s[6:7]
	v_cndmask_b32_e64 v3, v73, 11, s[10:11]
	v_cndmask_b32_e64 v74, v3, v74, s[68:69]
	v_cmp_gt_f32_e64 s[68:69], v13, v55
	v_cmp_gt_f32_e64 s[8:9], v13, v56
	v_cndmask_b32_e64 v84, v83, 20, s[2:3]
	v_cndmask_b32_e64 v3, v55, v13, s[68:69]
	v_cndmask_b32_e64 v57, v56, v13, s[8:9]
	v_cndmask_b32_e64 v56, v3, v56, s[8:9]
	v_cndmask_b32_e64 v3, v74, 12, s[44:45]
	v_cndmask_b32_e64 v75, v3, v75, s[70:71]
	s_waitcnt lgkmcnt(3)
	v_cmp_gt_f32_e64 s[70:71], v10, v56
	v_cmp_gt_f32_e64 s[14:15], v10, v57
	v_cndmask_b32_e64 v85, v84, 21, s[4:5]
	v_cndmask_b32_e64 v3, v56, v10, s[70:71]
	v_cndmask_b32_e64 v58, v57, v10, s[14:15]
	v_cndmask_b32_e64 v57, v3, v57, s[14:15]
	v_cndmask_b32_e64 v3, v75, 13, s[46:47]
	v_cndmask_b32_e64 v76, v3, v76, s[72:73]
	v_cmp_gt_f32_e64 s[72:73], v11, v57
	v_cmp_gt_f32_e64 s[20:21], v11, v58
	v_cndmask_b32_e64 v86, v85, 22, s[6:7]
	v_cndmask_b32_e64 v3, v57, v11, s[72:73]
	v_cndmask_b32_e64 v59, v58, v11, s[20:21]
	v_cndmask_b32_e64 v58, v3, v58, s[20:21]
	v_cndmask_b32_e64 v3, v76, 14, s[48:49]
	v_cndmask_b32_e64 v77, v3, v77, s[74:75]
	s_waitcnt lgkmcnt(2)
	v_cmp_gt_f32_e64 s[74:75], v8, v58
	v_cmp_gt_f32_e64 s[26:27], v8, v59
	v_cndmask_b32_e64 v87, v86, 23, s[8:9]
	v_cndmask_b32_e64 v3, v58, v8, s[74:75]
	v_cndmask_b32_e64 v60, v59, v8, s[26:27]
	v_cndmask_b32_e64 v59, v3, v59, s[26:27]
	v_cndmask_b32_e64 v3, v77, 15, s[50:51]
	v_cndmask_b32_e64 v78, v3, v78, s[76:77]
	v_cmp_gt_f32_e64 s[76:77], v9, v59
	v_cmp_gt_f32_e64 s[34:35], v9, v60
	v_cndmask_b32_e64 v88, v87, 24, s[14:15]
	v_cndmask_b32_e64 v3, v59, v9, s[76:77]
	v_cndmask_b32_e64 v61, v60, v9, s[34:35]
	v_cndmask_b32_e64 v60, v3, v60, s[34:35]
	v_cndmask_b32_e64 v3, v78, 16, s[52:53]
	v_cndmask_b32_e64 v79, v3, v79, s[78:79]
	s_waitcnt lgkmcnt(1)
	v_cmp_gt_f32_e64 s[78:79], v6, v60
	v_cmp_gt_f32_e64 s[36:37], v6, v61
	v_cndmask_b32_e64 v89, v88, 25, s[20:21]
	v_cndmask_b32_e64 v3, v60, v6, s[78:79]
	v_cndmask_b32_e64 v62, v61, v6, s[36:37]
	v_cndmask_b32_e64 v61, v3, v61, s[36:37]
	v_cndmask_b32_e64 v3, v79, 17, s[54:55]
	v_cndmask_b32_e64 v80, v3, v80, s[82:83]
	v_cmp_gt_f32_e64 s[82:83], v7, v61
	v_cmp_gt_f32_e64 s[42:43], v7, v62
	v_cndmask_b32_e64 v90, v89, 26, s[26:27]
	v_cndmask_b32_e64 v3, v61, v7, s[82:83]
	v_cndmask_b32_e64 v63, v62, v7, s[42:43]
	v_cndmask_b32_e64 v62, v3, v62, s[42:43]
	v_cndmask_b32_e64 v3, v80, 18, s[56:57]
	v_cndmask_b32_e64 v81, v3, v81, s[80:81]
	s_waitcnt lgkmcnt(0)
	v_cmp_gt_f32_e64 s[80:81], v4, v62
	v_cmp_gt_f32_e64 s[58:59], v4, v63
	v_cndmask_b32_e64 v91, v90, 27, s[34:35]
	v_cndmask_b32_e64 v3, v62, v4, s[80:81]
	v_cndmask_b32_e64 v64, v63, v4, s[58:59]
	v_cndmask_b32_e64 v63, v3, v63, s[58:59]
	v_cndmask_b32_e64 v3, v81, 19, s[60:61]
	v_cndmask_b32_e32 v82, v3, v82, vcc
	v_cndmask_b32_e64 v3, v82, 20, s[62:63]
	v_cndmask_b32_e64 v83, v3, v83, s[2:3]
	v_cndmask_b32_e64 v3, v83, 21, s[64:65]
	v_cndmask_b32_e64 v84, v3, v84, s[4:5]
	v_cndmask_b32_e64 v3, v84, 22, s[66:67]
	v_cndmask_b32_e64 v85, v3, v85, s[6:7]
	v_cndmask_b32_e64 v3, v85, 23, s[68:69]
	v_cndmask_b32_e64 v86, v3, v86, s[8:9]
	v_cndmask_b32_e64 v3, v86, 24, s[70:71]
	v_cndmask_b32_e64 v87, v3, v87, s[14:15]
	v_cndmask_b32_e64 v3, v87, 25, s[72:73]
	v_cndmask_b32_e64 v88, v3, v88, s[20:21]
	v_cndmask_b32_e64 v3, v88, 26, s[74:75]
	v_cndmask_b32_e64 v89, v3, v89, s[26:27]
	v_cndmask_b32_e64 v3, v89, 27, s[76:77]
	v_cndmask_b32_e64 v90, v3, v90, s[34:35]
	v_cndmask_b32_e64 v3, v90, 28, s[78:79]
	v_cndmask_b32_e64 v92, v91, 28, s[36:37]
	v_cndmask_b32_e64 v91, v3, v91, s[36:37]
	v_cndmask_b32_e64 v3, v91, 29, s[82:83]
	v_cmp_lg_f32_e64 s[34:35], s89, v32
	v_cndmask_b32_e64 v93, v92, 29, s[42:43]
	v_cndmask_b32_e64 v92, v3, v92, s[42:43]
	v_cndmask_b32_e64 v32, v241, v32, s[34:35]
	v_cndmask_b32_e64 v3, v92, 30, s[80:81]
	v_cmp_gt_f32_e32 vcc, v5, v63
	v_cndmask_b32_e64 v32, v32, v94, s[40:41]
	v_cndmask_b32_e64 v2, v93, 30, s[58:59]
	v_cndmask_b32_e64 v34, v3, v93, s[58:59]
	v_cmp_gt_f32_e64 s[2:3], v5, v64
	v_cndmask_b32_e32 v36, v63, v5, vcc
	v_cmp_gt_f32_e64 s[58:59], v33, v32
	v_cndmask_b32_e64 v35, v64, v5, s[2:3]
	v_cndmask_b32_e64 v36, v36, v64, s[2:3]
	v_cndmask_b32_e64 v64, v32, v33, s[58:59]
	v_cndmask_b32_e64 v64, v64, v95, s[38:39]
	v_cmp_gt_f32_e64 s[42:43], v30, v64
	v_cndmask_b32_e64 v3, v34, 31, vcc
	v_cndmask_b32_e64 v3, v3, v2, s[2:3]
	v_cndmask_b32_e64 v93, v64, v30, s[42:43]
	v_cndmask_b32_e64 v93, v93, v96, s[30:31]
	v_cmp_gt_f32_e64 s[36:37], v31, v93
	v_cndmask_b32_e64 v2, v2, 31, s[2:3]
	v_readlane_b32 s2, v255, 40
	v_cndmask_b32_e64 v94, v93, v31, s[36:37]
	v_cndmask_b32_e64 v37, v94, v37, s[28:29]
	v_cmp_gt_f32_e64 s[26:27], v28, v37
	v_readlane_b32 s3, v255, 41
	s_nop 0
	v_cndmask_b32_e64 v94, v37, v28, s[26:27]
	v_cndmask_b32_e64 v38, v94, v38, s[24:25]
	v_cmp_gt_f32_e64 s[20:21], v29, v38
	s_nop 1
	v_cndmask_b32_e64 v94, v38, v29, s[20:21]
	v_cndmask_b32_e64 v39, v94, v39, s[22:23]
	v_cmp_gt_f32_e64 s[14:15], v26, v39
	s_nop 1
	v_cndmask_b32_e64 v94, v39, v26, s[14:15]
	v_cndmask_b32_e64 v40, v94, v40, s[18:19]
	v_cmp_gt_f32_e64 s[8:9], v27, v40
	s_nop 1
	v_cndmask_b32_e64 v94, v40, v27, s[8:9]
	v_cndmask_b32_e64 v41, v94, v41, s[16:17]
	v_cmp_gt_f32_e64 s[6:7], v24, v41
	s_nop 1
	v_cndmask_b32_e64 v94, v41, v24, s[6:7]
	v_cndmask_b32_e64 v42, v94, v42, s[12:13]
	v_cmp_gt_f32_e64 s[4:5], v25, v42
	s_nop 1
	v_cndmask_b32_e64 v94, v42, v25, s[4:5]
	v_cndmask_b32_e64 v43, v94, v43, s[10:11]
	v_cndmask_b32_e64 v94, 0, 2, s[34:35]
	v_cmp_gt_f32_e64 s[34:35], v22, v43
	v_cndmask_b32_e64 v94, v94, v97, s[40:41]
	s_nop 0
	v_cndmask_b32_e64 v95, v43, v22, s[34:35]
	v_cndmask_b32_e64 v44, v95, v44, s[44:45]
	v_cmp_gt_f32_e64 s[40:41], v23, v44
	s_nop 1
	v_cndmask_b32_e64 v95, v44, v23, s[40:41]
	v_cndmask_b32_e64 v45, v95, v45, s[46:47]
	v_cndmask_b32_e64 v95, v94, 3, s[58:59]
	v_cndmask_b32_e64 v65, v95, v65, s[38:39]
	v_cmp_gt_f32_e64 s[38:39], v20, v45
	s_nop 1
	v_cndmask_b32_e64 v95, v45, v20, s[38:39]
	v_cndmask_b32_e64 v46, v95, v46, s[48:49]
	v_cndmask_b32_e64 v95, v65, 4, s[42:43]
	v_cndmask_b32_e64 v66, v95, v66, s[30:31]
	v_cmp_gt_f32_e64 s[30:31], v21, v46
	s_nop 1
	v_cndmask_b32_e64 v95, v46, v21, s[30:31]
	v_cndmask_b32_e64 v47, v95, v47, s[50:51]
	v_cndmask_b32_e64 v95, v66, 5, s[36:37]
	v_cndmask_b32_e64 v67, v95, v67, s[28:29]
	v_cmp_gt_f32_e64 s[28:29], v18, v47
	s_nop 1
	v_cndmask_b32_e64 v95, v47, v18, s[28:29]
	v_cndmask_b32_e64 v48, v95, v48, s[52:53]
	v_cndmask_b32_e64 v95, v67, 6, s[26:27]
	v_cndmask_b32_e64 v68, v95, v68, s[24:25]
	v_cmp_gt_f32_e64 s[24:25], v19, v48
	s_nop 1
	v_cndmask_b32_e64 v95, v48, v19, s[24:25]
	v_cndmask_b32_e64 v49, v95, v49, s[54:55]
	v_cndmask_b32_e64 v95, v68, 7, s[20:21]
	v_cndmask_b32_e64 v69, v95, v69, s[22:23]
	v_cmp_gt_f32_e64 s[22:23], v16, v49
	s_nop 1
	v_cndmask_b32_e64 v95, v49, v16, s[22:23]
	v_cndmask_b32_e64 v50, v95, v50, s[56:57]
	v_cndmask_b32_e64 v95, v69, 8, s[14:15]
	v_cndmask_b32_e64 v70, v95, v70, s[18:19]
	v_cmp_gt_f32_e64 s[18:19], v17, v50
	s_nop 1
	v_cndmask_b32_e64 v95, v50, v17, s[18:19]
	v_cndmask_b32_e64 v51, v95, v51, s[60:61]
	v_cndmask_b32_e64 v95, v70, 9, s[8:9]
	v_cndmask_b32_e64 v71, v95, v71, s[16:17]
	v_cmp_gt_f32_e64 s[16:17], v14, v51
	s_nop 1
	v_cndmask_b32_e64 v95, v51, v14, s[16:17]
	v_cndmask_b32_e64 v52, v95, v52, s[62:63]
	v_cndmask_b32_e64 v95, v71, 10, s[6:7]
	v_cndmask_b32_e64 v72, v95, v72, s[12:13]
	v_cmp_gt_f32_e64 s[12:13], v15, v52
	s_nop 1
	v_cndmask_b32_e64 v95, v52, v15, s[12:13]
	v_cndmask_b32_e64 v53, v95, v53, s[64:65]
	v_cndmask_b32_e64 v95, v72, 11, s[4:5]
	v_cndmask_b32_e64 v73, v95, v73, s[10:11]
	v_cmp_gt_f32_e64 s[10:11], v12, v53
	s_nop 1
	v_cndmask_b32_e64 v95, v53, v12, s[10:11]
	v_cndmask_b32_e64 v54, v95, v54, s[66:67]
	v_cndmask_b32_e64 v95, v73, 12, s[34:35]
	v_cndmask_b32_e64 v74, v95, v74, s[44:45]
	v_cmp_gt_f32_e64 s[44:45], v13, v54
	s_nop 1
	v_cndmask_b32_e64 v95, v54, v13, s[44:45]
	v_cndmask_b32_e64 v55, v95, v55, s[68:69]
	v_cndmask_b32_e64 v95, v74, 13, s[40:41]
	v_cndmask_b32_e64 v75, v95, v75, s[46:47]
	v_cmp_gt_f32_e64 s[46:47], v10, v55
	s_nop 1
	v_cndmask_b32_e64 v95, v55, v10, s[46:47]
	v_cndmask_b32_e64 v56, v95, v56, s[70:71]
	v_cndmask_b32_e64 v95, v75, 14, s[38:39]
	v_cndmask_b32_e64 v76, v95, v76, s[48:49]
	v_cmp_gt_f32_e64 s[48:49], v11, v56
	s_nop 1
	v_cndmask_b32_e64 v95, v56, v11, s[48:49]
	v_cndmask_b32_e64 v57, v95, v57, s[72:73]
	v_cndmask_b32_e64 v95, v76, 15, s[30:31]
	v_cndmask_b32_e64 v77, v95, v77, s[50:51]
	v_cmp_gt_f32_e64 s[50:51], v8, v57
	s_nop 1
	v_cndmask_b32_e64 v95, v57, v8, s[50:51]
	v_cndmask_b32_e64 v58, v95, v58, s[74:75]
	v_cndmask_b32_e64 v95, v77, 16, s[28:29]
	v_cndmask_b32_e64 v78, v95, v78, s[52:53]
	v_cmp_gt_f32_e64 s[52:53], v9, v58
	s_nop 1
	v_cndmask_b32_e64 v95, v58, v9, s[52:53]
	v_cndmask_b32_e64 v59, v95, v59, s[76:77]
	v_cndmask_b32_e64 v95, v78, 17, s[24:25]
	v_cndmask_b32_e64 v79, v95, v79, s[54:55]
	v_cmp_gt_f32_e64 s[54:55], v6, v59
	s_nop 1
	v_cndmask_b32_e64 v95, v59, v6, s[54:55]
	v_cndmask_b32_e64 v60, v95, v60, s[78:79]
	v_cndmask_b32_e64 v95, v79, 18, s[22:23]
	v_cndmask_b32_e64 v80, v95, v80, s[56:57]
	v_cmp_gt_f32_e64 s[56:57], v7, v60
	s_nop 1
	v_cndmask_b32_e64 v95, v60, v7, s[56:57]
	v_cndmask_b32_e64 v61, v95, v61, s[82:83]
	v_cndmask_b32_e64 v95, v80, 19, s[18:19]
	v_cndmask_b32_e64 v81, v95, v81, s[60:61]
	v_cmp_gt_f32_e64 s[60:61], v4, v61
	s_nop 1
	v_cndmask_b32_e64 v95, v61, v4, s[60:61]
	v_cndmask_b32_e64 v62, v95, v62, s[80:81]
	v_cndmask_b32_e64 v95, v81, 20, s[16:17]
	v_cndmask_b32_e64 v82, v95, v82, s[62:63]
	v_cndmask_b32_e64 v95, v82, 21, s[12:13]
	v_cndmask_b32_e64 v83, v95, v83, s[64:65]
	v_cndmask_b32_e64 v95, v83, 22, s[10:11]
	v_cndmask_b32_e64 v84, v95, v84, s[66:67]
	v_cndmask_b32_e64 v95, v84, 23, s[44:45]
	v_cndmask_b32_e64 v85, v95, v85, s[68:69]
	v_cndmask_b32_e64 v95, v85, 24, s[46:47]
	v_cndmask_b32_e64 v86, v95, v86, s[70:71]
	v_cndmask_b32_e64 v95, v86, 25, s[48:49]
	v_cndmask_b32_e64 v87, v95, v87, s[72:73]
	v_cndmask_b32_e64 v95, v87, 26, s[50:51]
	v_cndmask_b32_e64 v88, v95, v88, s[74:75]
	v_cndmask_b32_e64 v95, v88, 27, s[52:53]
	v_cndmask_b32_e64 v89, v95, v89, s[76:77]
	v_cndmask_b32_e64 v95, v89, 28, s[54:55]
	v_cndmask_b32_e64 v90, v95, v90, s[78:79]
	v_cndmask_b32_e64 v95, v90, 29, s[56:57]
	v_cmp_lg_f32_e64 s[78:79], s89, v33
	v_cndmask_b32_e64 v91, v95, v91, s[82:83]
	v_cndmask_b32_e64 v95, v91, 30, s[60:61]
	v_cndmask_b32_e64 v33, v241, v33, s[78:79]
	v_cndmask_b32_e64 v32, v33, v32, s[58:59]
	v_cndmask_b32_e64 v92, v95, v92, s[80:81]
	v_cmp_gt_f32_e64 s[80:81], v30, v32
	v_cmp_gt_f32_e64 s[62:63], v5, v62
	s_nop 0
	v_cndmask_b32_e64 v30, v32, v30, s[80:81]
	v_cndmask_b32_e64 v30, v30, v64, s[42:43]
	v_cmp_gt_f32_e64 s[82:83], v31, v30
	v_cndmask_b32_e64 v96, v62, v5, s[62:63]
	v_cndmask_b32_e32 v63, v96, v63, vcc
	v_cndmask_b32_e64 v30, v30, v31, s[82:83]
	v_cndmask_b32_e64 v30, v30, v93, s[36:37]
	v_cmp_gt_f32_e64 s[76:77], v28, v30
	v_cndmask_b32_e64 v95, v92, 31, s[62:63]
	s_nop 0
	v_cndmask_b32_e64 v28, v30, v28, s[76:77]
	v_cndmask_b32_e64 v28, v28, v37, s[26:27]
	v_cmp_gt_f32_e64 s[74:75], v29, v28
	s_nop 1
	v_cndmask_b32_e64 v28, v28, v29, s[74:75]
	v_cndmask_b32_e64 v28, v28, v38, s[20:21]
	v_cmp_gt_f32_e64 s[72:73], v26, v28
	s_nop 1
	v_cndmask_b32_e64 v26, v28, v26, s[72:73]
	v_cndmask_b32_e64 v26, v26, v39, s[14:15]
	v_cmp_gt_f32_e64 s[70:71], v27, v26
	s_nop 1
	v_cndmask_b32_e64 v26, v26, v27, s[70:71]
	v_cndmask_b32_e64 v26, v26, v40, s[8:9]
	v_cmp_gt_f32_e64 s[68:69], v24, v26
	s_nop 1
	v_cndmask_b32_e64 v24, v26, v24, s[68:69]
	v_cndmask_b32_e64 v24, v24, v41, s[6:7]
	v_cmp_gt_f32_e64 s[66:67], v25, v24
	s_nop 1
	v_cndmask_b32_e64 v24, v24, v25, s[66:67]
	v_cndmask_b32_e64 v24, v24, v42, s[4:5]
	v_cmp_gt_f32_e64 s[64:65], v22, v24
	s_nop 1
	v_cndmask_b32_e64 v22, v24, v22, s[64:65]
	v_cndmask_b32_e64 v22, v22, v43, s[34:35]
	v_cndmask_b32_e64 v24, 0, 3, s[78:79]
	v_cmp_gt_f32_e64 s[78:79], v23, v22
	s_nop 1
	v_cndmask_b32_e64 v22, v22, v23, s[78:79]
	v_cndmask_b32_e64 v22, v22, v44, s[40:41]
	v_cndmask_b32_e64 v23, v24, v94, s[58:59]
	v_cmp_gt_f32_e64 s[58:59], v20, v22
	s_nop 1
	v_cndmask_b32_e64 v20, v22, v20, s[58:59]
	v_cndmask_b32_e64 v20, v20, v45, s[38:39]
	v_cndmask_b32_e64 v22, v23, 4, s[80:81]
	v_cmp_gt_f32_e64 s[80:81], v21, v20
	s_nop 1
	v_cndmask_b32_e64 v20, v20, v21, s[80:81]
	v_cndmask_b32_e64 v20, v20, v46, s[30:31]
	v_cndmask_b32_e64 v21, v22, v65, s[42:43]
	v_cmp_gt_f32_e64 s[42:43], v18, v20
	s_nop 1
	v_cndmask_b32_e64 v18, v20, v18, s[42:43]
	v_cndmask_b32_e64 v18, v18, v47, s[28:29]
	v_cndmask_b32_e64 v20, v21, 5, s[82:83]
	v_cmp_gt_f32_e64 s[82:83], v19, v18
	s_nop 1
	v_cndmask_b32_e64 v18, v18, v19, s[82:83]
	v_cndmask_b32_e64 v18, v18, v48, s[24:25]
	v_cndmask_b32_e64 v19, v20, v66, s[36:37]
	v_cmp_gt_f32_e64 s[36:37], v16, v18
	s_nop 1
	v_cndmask_b32_e64 v16, v18, v16, s[36:37]
	v_cndmask_b32_e64 v16, v16, v49, s[22:23]
	v_cndmask_b32_e64 v18, v19, 6, s[76:77]
	v_cmp_gt_f32_e64 s[76:77], v17, v16
	s_nop 1
	v_cndmask_b32_e64 v16, v16, v17, s[76:77]
	v_cndmask_b32_e64 v16, v16, v50, s[18:19]
	v_cndmask_b32_e64 v17, v18, v67, s[26:27]
	v_cmp_gt_f32_e64 s[26:27], v14, v16
	s_nop 1
	v_cndmask_b32_e64 v14, v16, v14, s[26:27]
	v_cndmask_b32_e64 v14, v14, v51, s[16:17]
	v_cndmask_b32_e64 v16, v17, 7, s[74:75]
	v_cmp_gt_f32_e64 s[74:75], v15, v14
	s_nop 1
	v_cndmask_b32_e64 v14, v14, v15, s[74:75]
	v_cndmask_b32_e64 v14, v14, v52, s[12:13]
	v_cndmask_b32_e64 v15, v16, v68, s[20:21]
	v_cmp_gt_f32_e64 s[20:21], v12, v14
	s_nop 1
	v_cndmask_b32_e64 v12, v14, v12, s[20:21]
	v_cndmask_b32_e64 v12, v12, v53, s[10:11]
	v_cndmask_b32_e64 v14, v15, 8, s[72:73]
	v_cmp_gt_f32_e64 s[72:73], v13, v12
	s_nop 1
	v_cndmask_b32_e64 v12, v12, v13, s[72:73]
	v_cndmask_b32_e64 v12, v12, v54, s[44:45]
	v_cndmask_b32_e64 v13, v14, v69, s[14:15]
	v_cmp_gt_f32_e64 s[14:15], v10, v12
	s_nop 1
	v_cndmask_b32_e64 v10, v12, v10, s[14:15]
	v_cndmask_b32_e64 v10, v10, v55, s[46:47]
	v_cndmask_b32_e64 v12, v13, 9, s[70:71]
	v_cmp_gt_f32_e64 s[70:71], v11, v10
	s_nop 1
	v_cndmask_b32_e64 v10, v10, v11, s[70:71]
	v_cndmask_b32_e64 v10, v10, v56, s[48:49]
	v_cndmask_b32_e64 v11, v12, v70, s[8:9]
	v_cmp_gt_f32_e64 s[8:9], v8, v10
	s_nop 1
	v_cndmask_b32_e64 v8, v10, v8, s[8:9]
	v_cndmask_b32_e64 v8, v8, v57, s[50:51]
	v_cndmask_b32_e64 v10, v11, 10, s[68:69]
	v_cmp_gt_f32_e64 s[68:69], v9, v8
	s_nop 1
	v_cndmask_b32_e64 v8, v8, v9, s[68:69]
	v_cndmask_b32_e64 v8, v8, v58, s[52:53]
	v_cndmask_b32_e64 v9, v10, v71, s[6:7]
	v_cmp_gt_f32_e64 s[6:7], v6, v8
	s_nop 1
	v_cndmask_b32_e64 v6, v8, v6, s[6:7]
	v_cndmask_b32_e64 v6, v6, v59, s[54:55]
	v_cndmask_b32_e64 v8, v9, 11, s[66:67]
	v_cmp_gt_f32_e64 s[66:67], v7, v6
	s_nop 1
	v_cndmask_b32_e64 v6, v6, v7, s[66:67]
	v_cndmask_b32_e64 v6, v6, v60, s[56:57]
	v_cndmask_b32_e64 v7, v8, v72, s[4:5]
	v_cmp_gt_f32_e64 s[4:5], v4, v6
	s_nop 1
	v_cndmask_b32_e64 v4, v6, v4, s[4:5]
	v_cndmask_b32_e64 v6, v7, 12, s[64:65]
	v_cndmask_b32_e64 v6, v6, v73, s[34:35]
	v_cndmask_b32_e64 v6, v6, 13, s[78:79]
	v_cndmask_b32_e64 v6, v6, v74, s[40:41]
	v_cndmask_b32_e64 v6, v6, 14, s[58:59]
	v_cndmask_b32_e64 v6, v6, v75, s[38:39]
	v_cndmask_b32_e64 v6, v6, 15, s[80:81]
	v_cndmask_b32_e64 v6, v6, v76, s[30:31]
	v_cndmask_b32_e64 v6, v6, 16, s[42:43]
	v_cndmask_b32_e64 v6, v6, v77, s[28:29]
	v_cndmask_b32_e64 v6, v6, 17, s[82:83]
	v_cndmask_b32_e64 v6, v6, v78, s[24:25]
	v_cndmask_b32_e64 v6, v6, 18, s[36:37]
	v_cndmask_b32_e64 v6, v6, v79, s[22:23]
	v_cndmask_b32_e64 v6, v6, 19, s[76:77]
	v_cndmask_b32_e64 v6, v6, v80, s[18:19]
	v_cndmask_b32_e64 v6, v6, 20, s[26:27]
	v_cndmask_b32_e64 v6, v6, v81, s[16:17]
	v_cndmask_b32_e64 v6, v6, 21, s[74:75]
	v_cndmask_b32_e64 v6, v6, v82, s[12:13]
	v_cndmask_b32_e64 v6, v6, 22, s[20:21]
	v_cndmask_b32_e64 v6, v6, v83, s[10:11]
	v_cndmask_b32_e64 v6, v6, 23, s[72:73]
	v_cndmask_b32_e64 v6, v6, v84, s[44:45]
	v_cndmask_b32_e64 v6, v6, 24, s[14:15]
	v_cndmask_b32_e64 v6, v6, v85, s[46:47]
	v_cndmask_b32_e64 v6, v6, 25, s[70:71]
	v_cndmask_b32_e64 v6, v6, v86, s[48:49]
	v_cndmask_b32_e64 v6, v6, 26, s[8:9]
	v_cndmask_b32_e64 v6, v6, v87, s[50:51]
	v_cndmask_b32_e64 v6, v6, 27, s[68:69]
	v_cndmask_b32_e64 v6, v6, v88, s[52:53]
	v_cndmask_b32_e64 v6, v6, 28, s[6:7]
	v_cndmask_b32_e64 v6, v6, v89, s[54:55]
	v_cndmask_b32_e64 v6, v6, 29, s[66:67]
	v_cndmask_b32_e64 v4, v4, v61, s[60:61]
	v_cndmask_b32_e64 v6, v6, v90, s[56:57]
	v_cndmask_b32_e64 v6, v6, 30, s[4:5]
	v_cmp_gt_f32_e64 s[4:5], v5, v4
	v_sub_f32_e32 v7, v36, v35
	v_mul_f32_e32 v7, 0x3fb8aa3b, v7
	v_cndmask_b32_e64 v4, v4, v5, s[4:5]
	v_cndmask_b32_e64 v4, v4, v62, s[62:63]
	v_sub_f32_e32 v5, v63, v35
	v_sub_f32_e32 v4, v4, v35
	v_mul_f32_e32 v5, 0x3fb8aa3b, v5
	v_exp_f32_e32 v8, v7
	v_mul_f32_e32 v4, 0x3fb8aa3b, v4
	v_exp_f32_e32 v9, v5
	v_exp_f32_e32 v7, v4
	v_add_f32_e32 v4, 1.0, v8
	v_cndmask_b32_e64 v6, v6, v91, s[60:61]
	v_add_f32_e32 v4, v9, v4
	v_cndmask_b32_e64 v5, v6, 31, s[4:5]
	v_add_f32_e32 v6, v7, v4
	v_div_scale_f32 v10, s[4:5], v6, v6, 1.0
	v_rcp_f32_e32 v11, v10
	v_cndmask_b32_e32 v4, v95, v34, vcc
	v_cndmask_b32_e64 v5, v5, v92, s[62:63]
	v_readlane_b32 s76, v255, 27
	v_fma_f32 v12, -v10, v11, 1.0
	v_fmac_f32_e32 v11, v12, v11
	v_div_scale_f32 v12, vcc, 1.0, v6, 1.0
	v_mul_f32_e32 v13, v12, v11
	v_fma_f32 v14, -v10, v13, v12
	v_fmac_f32_e32 v13, v14, v11
	v_fma_f32 v10, -v10, v13, v12
	v_div_fmas_f32 v10, v10, v11, v13
	v_div_fixup_f32 v6, v10, v6, 1.0
	v_lshlrev_b64 v[10:11], 4, v[162:163]
	v_lshl_add_u64 v[12:13], s[2:3], 0, v[10:11]
	v_readlane_b32 s2, v255, 42
	global_store_dwordx4 v[12:13], v[2:5], off
	v_pk_mul_f32 v[12:13], v[8:9], v[6:7] op_sel_hi:[1,0]
	v_readlane_b32 s3, v255, 43
	v_mul_f32_e32 v9, v7, v6
	v_mov_b32_e32 v7, v12
	v_lshl_add_u64 v[10:11], s[2:3], 0, v[10:11]
	v_mov_b32_e32 v8, v13
	global_store_dwordx4 v[10:11], v[6:9], off
	v_lshl_add_u32 v2, v2, 2, s86
	ds_add_u32 v2, v239
	v_lshl_add_u32 v2, v3, 2, s86
	ds_add_u32 v2, v239
	v_lshl_add_u32 v2, v4, 2, s86
	ds_add_u32 v2, v239
	v_lshl_add_u32 v2, v5, 2, s86
	ds_add_u32 v2, v239
	v_readlane_b32 s56, v255, 23
	v_readlane_b32 s78, v255, 29
	v_readlane_b32 s79, v255, 30
	v_readlane_b32 s80, v255, 31
	v_readlane_b32 s81, v255, 32
	v_readlane_b32 s82, v255, 33
	v_readlane_b32 s83, v255, 34
	s_mov_b32 s76, s87
	v_readlane_b32 s57, v255, 24
	v_readlane_b32 s77, v255, 28
	v_readlane_b32 s58, v255, 25
	v_readlane_b32 s59, v255, 26
	s_branch .LBB0_931
